# v36 + GEMM K-loops: B/A fragment LDS read addresses use precomputed base VGPR + immediate offset (16 v_add per trip removed), redundant s_setprio 0/1 pairs removed
# speedup vs baseline: 1.0108x; 1.0078x over previous
.LBB0_176:
	s_add_u32 s56, s26, 0x100
	s_addc_u32 s57, s27, 0
	v_mov_b32_e32 v167, v165
	v_mov_b32_e32 v169, v165
	s_add_u32 s58, s28, 0x100
	v_mov_b32_e32 v32, 0
	v_mov_b32_e32 v175, v165
	v_mov_b32_e32 v177, v165
	v_lshl_add_u64 v[178:179], s[16:17], 0, v[168:169]
	v_lshl_add_u64 v[180:181], s[16:17], 0, v[166:167]
	s_addc_u32 s59, s29, 0
	s_mov_b32 s60, -2
	s_mov_b64 s[26:27], 0
	v_mov_b32_e32 v33, v32
	v_mov_b32_e32 v34, v32
	v_mov_b32_e32 v35, v32
	v_mov_b32_e32 v36, v32
	v_mov_b32_e32 v37, v32
	v_mov_b32_e32 v38, v32
	v_mov_b32_e32 v39, v32
	v_mov_b32_e32 v44, v32
	v_mov_b32_e32 v45, v32
	v_mov_b32_e32 v46, v32
	v_mov_b32_e32 v47, v32
	v_mov_b32_e32 v52, v32
	v_mov_b32_e32 v53, v32
	v_mov_b32_e32 v54, v32
	v_mov_b32_e32 v55, v32
	v_mov_b32_e32 v60, v32
	v_mov_b32_e32 v61, v32
	v_mov_b32_e32 v62, v32
	v_mov_b32_e32 v63, v32
	v_mov_b32_e32 v68, v32
	v_mov_b32_e32 v69, v32
	v_mov_b32_e32 v70, v32
	v_mov_b32_e32 v71, v32
	v_mov_b32_e32 v76, v32
	v_mov_b32_e32 v77, v32
	v_mov_b32_e32 v78, v32
	v_mov_b32_e32 v79, v32
	v_mov_b32_e32 v84, v32
	v_mov_b32_e32 v85, v32
	v_mov_b32_e32 v86, v32
	v_mov_b32_e32 v87, v32
	v_mov_b32_e32 v40, v32
	v_mov_b32_e32 v41, v32
	v_mov_b32_e32 v42, v32
	v_mov_b32_e32 v43, v32
	v_mov_b32_e32 v48, v32
	v_mov_b32_e32 v49, v32
	v_mov_b32_e32 v50, v32
	v_mov_b32_e32 v51, v32
	v_mov_b32_e32 v56, v32
	v_mov_b32_e32 v57, v32
	v_mov_b32_e32 v58, v32
	v_mov_b32_e32 v59, v32
	v_mov_b32_e32 v64, v32
	v_mov_b32_e32 v65, v32
	v_mov_b32_e32 v66, v32
	v_mov_b32_e32 v67, v32
	v_mov_b32_e32 v72, v32
	v_mov_b32_e32 v73, v32
	v_mov_b32_e32 v74, v32
	v_mov_b32_e32 v75, v32
	v_mov_b32_e32 v80, v32
	v_mov_b32_e32 v81, v32
	v_mov_b32_e32 v82, v32
	v_mov_b32_e32 v83, v32
	v_mov_b32_e32 v88, v32
	v_mov_b32_e32 v89, v32
	v_mov_b32_e32 v90, v32
	v_mov_b32_e32 v91, v32
	v_mov_b32_e32 v92, v32
	v_mov_b32_e32 v93, v32
	v_mov_b32_e32 v94, v32
	v_mov_b32_e32 v95, v32
	v_mov_b32_e32 v96, v32
	v_mov_b32_e32 v97, v32
	v_mov_b32_e32 v98, v32
	v_mov_b32_e32 v99, v32
	v_mov_b32_e32 v100, v32
	v_mov_b32_e32 v101, v32
	v_mov_b32_e32 v102, v32
	v_mov_b32_e32 v103, v32
	v_mov_b32_e32 v108, v32
	v_mov_b32_e32 v109, v32
	v_mov_b32_e32 v110, v32
	v_mov_b32_e32 v111, v32
	v_mov_b32_e32 v116, v32
	v_mov_b32_e32 v117, v32
	v_mov_b32_e32 v118, v32
	v_mov_b32_e32 v119, v32
	v_mov_b32_e32 v124, v32
	v_mov_b32_e32 v125, v32
	v_mov_b32_e32 v126, v32
	v_mov_b32_e32 v127, v32
	v_mov_b32_e32 v132, v32
	v_mov_b32_e32 v133, v32
	v_mov_b32_e32 v134, v32
	v_mov_b32_e32 v135, v32
	v_mov_b32_e32 v140, v32
	v_mov_b32_e32 v141, v32
	v_mov_b32_e32 v142, v32
	v_mov_b32_e32 v143, v32
	v_mov_b32_e32 v148, v32
	v_mov_b32_e32 v149, v32
	v_mov_b32_e32 v150, v32
	v_mov_b32_e32 v151, v32
	v_mov_b32_e32 v104, v32
	v_mov_b32_e32 v105, v32
	v_mov_b32_e32 v106, v32
	v_mov_b32_e32 v107, v32
	v_mov_b32_e32 v112, v32
	v_mov_b32_e32 v113, v32
	v_mov_b32_e32 v114, v32
	v_mov_b32_e32 v115, v32
	v_mov_b32_e32 v120, v32
	v_mov_b32_e32 v121, v32
	v_mov_b32_e32 v122, v32
	v_mov_b32_e32 v123, v32
	v_mov_b32_e32 v128, v32
	v_mov_b32_e32 v129, v32
	v_mov_b32_e32 v130, v32
	v_mov_b32_e32 v131, v32
	v_mov_b32_e32 v136, v32
	v_mov_b32_e32 v137, v32
	v_mov_b32_e32 v138, v32
	v_mov_b32_e32 v139, v32
	v_mov_b32_e32 v144, v32
	v_mov_b32_e32 v145, v32
	v_mov_b32_e32 v146, v32
	v_mov_b32_e32 v147, v32
	v_mov_b32_e32 v152, v32
	v_mov_b32_e32 v153, v32
	v_mov_b32_e32 v154, v32
	v_mov_b32_e32 v155, v32
	v_mov_b32_e32 v156, v32
	v_mov_b32_e32 v157, v32
	v_mov_b32_e32 v158, v32
	v_mov_b32_e32 v159, v32
	v_add_u32_e32 v252, 0x10000, v204
	v_add_u32_e32 v253, 0x10000, v205
	s_branch .LBB0_178
.LBB0_177:
	s_add_u32 s28, s4, s26
	s_addc_u32 s29, s5, s27
	s_add_u32 s30, s28, 0xe000100
	s_addc_u32 s31, s29, 0
	ds_read_b128 v[24:27], v252
	ds_read_b128 v[28:31], v253
	s_and_b64 s[28:29], s[34:35], exec
	ds_read_b128 v[16:19], v252 offset:2048
	ds_read_b128 v[20:23], v253 offset:2048
	s_cselect_b32 s29, s7, s31
	s_cselect_b32 s28, s6, s30
	s_add_u32 s61, s56, s26
	ds_read_b128 v[8:11], v252 offset:16384
	ds_read_b128 v[12:15], v253 offset:16384
	s_addc_u32 s62, s57, s27
	ds_read_b128 v[0:3], v252 offset:18432
	ds_read_b128 v[4:7], v253 offset:18432
	s_and_b64 s[30:31], s[34:35], exec
	s_cselect_b32 s31, s23, s62
	s_cselect_b32 s30, s22, s61
	s_add_u32 s61, s58, s26
	s_addc_u32 s62, s59, s27
	s_and_b64 s[34:35], s[34:35], exec
	s_cselect_b32 s35, s25, s62
	s_cselect_b32 s34, s24, s61
	v_lshl_add_u64 v[194:195], v[180:181], 0, s[26:27]
	s_add_i32 m0, s37, 0xc000
	ds_read_b128 v[186:189], v206
	ds_read_b128 v[214:217], v206 offset:2048
	ds_read_b128 v[190:193], v207
	ds_read_b128 v[218:221], v207 offset:2048
	ds_read_b128 v[222:225], v206 offset:4096
	ds_read_b128 v[230:233], v206 offset:6144
	ds_read_b128 v[226:229], v207 offset:4096
	ds_read_b128 v[234:237], v207 offset:6144
	global_load_lds_dwordx4 v[194:195], off
	v_lshl_add_u64 v[194:195], v[178:179], 0, s[26:27]
	s_add_i32 m0, s37, 0xe000
	s_nop 0
	global_load_lds_dwordx4 v[194:195], off
	s_waitcnt vmcnt(8)
	s_waitcnt lgkmcnt(0)
	s_barrier
	s_setprio 1
	s_waitcnt lgkmcnt(0)
	v_mfma_f32_16x16x128_f8f6f4 v[156:159], v[24:31], v[186:193], v[156:159]
	v_mfma_f32_16x16x128_f8f6f4 v[152:155], v[16:23], v[186:193], v[152:155]
	v_mfma_f32_16x16x128_f8f6f4 v[144:147], v[24:31], v[214:221], v[144:147]
	v_mfma_f32_16x16x128_f8f6f4 v[136:139], v[16:23], v[214:221], v[136:139]
	v_mfma_f32_16x16x128_f8f6f4 v[128:131], v[24:31], v[222:229], v[128:131]
	v_mfma_f32_16x16x128_f8f6f4 v[120:123], v[16:23], v[222:229], v[120:123]
	v_mfma_f32_16x16x128_f8f6f4 v[112:115], v[24:31], v[230:237], v[112:115]
	v_mfma_f32_16x16x128_f8f6f4 v[104:107], v[16:23], v[230:237], v[104:107]
	v_mfma_f32_16x16x128_f8f6f4 v[148:151], v[8:15], v[186:193], v[148:151]
	v_mfma_f32_16x16x128_f8f6f4 v[140:143], v[0:7], v[186:193], v[140:143]
	v_mfma_f32_16x16x128_f8f6f4 v[132:135], v[8:15], v[214:221], v[132:135]
	v_mfma_f32_16x16x128_f8f6f4 v[124:127], v[0:7], v[214:221], v[124:127]
	v_mfma_f32_16x16x128_f8f6f4 v[116:119], v[8:15], v[222:229], v[116:119]
	v_mfma_f32_16x16x128_f8f6f4 v[108:111], v[0:7], v[222:229], v[108:111]
	v_mfma_f32_16x16x128_f8f6f4 v[100:103], v[8:15], v[230:237], v[100:103]
	v_mfma_f32_16x16x128_f8f6f4 v[96:99], v[0:7], v[230:237], v[96:99]
	s_setprio 0
	s_barrier
	s_add_i32 s61, s44, s36
	v_lshl_add_u64 v[186:187], s[30:31], 0, v[160:161]
	s_mov_b32 m0, s61
	ds_read_b128 v[214:217], v206 offset:16384
	ds_read_b128 v[222:225], v206 offset:18432
	ds_read_b128 v[218:221], v207 offset:16384
	ds_read_b128 v[226:229], v207 offset:18432
	ds_read_b128 v[230:233], v206 offset:20480
	ds_read_b128 v[238:241], v206 offset:22528
	ds_read_b128 v[234:237], v207 offset:20480
	ds_read_b128 v[242:245], v207 offset:22528
	global_load_lds_dwordx4 v[186:187], off
	v_lshl_add_u64 v[188:189], s[30:31], 0, v[162:163]
	s_add_i32 m0, s61, 0x2000
	s_add_i32 s30, s46, s36
	global_load_lds_dwordx4 v[188:189], off
	v_lshl_add_u64 v[190:191], s[34:35], 0, v[160:161]
	s_mov_b32 m0, s30
	v_lshl_add_u64 v[192:193], s[34:35], 0, v[162:163]
	global_load_lds_dwordx4 v[190:191], off
	s_add_i32 m0, s30, 0x2000
	v_mov_b32_e32 v173, v165
	global_load_lds_dwordx4 v[192:193], off
	s_mov_b32 m0, s37
	v_lshl_add_u64 v[196:197], s[28:29], 0, v[164:165]
	global_load_lds_dwordx4 v164, s[28:29]
	s_mov_b32 m0, s38
	v_lshl_add_u64 v[194:195], s[28:29], 0, v[172:173]
	global_load_lds_dwordx4 v172, s[28:29]
	s_waitcnt vmcnt(8)
	s_waitcnt lgkmcnt(0)
	s_barrier
	s_setprio 1
	s_waitcnt lgkmcnt(0)
	v_mfma_f32_16x16x128_f8f6f4 v[92:95], v[24:31], v[214:221], v[92:95]
	v_mfma_f32_16x16x128_f8f6f4 v[88:91], v[16:23], v[214:221], v[88:91]
	v_mfma_f32_16x16x128_f8f6f4 v[80:83], v[24:31], v[222:229], v[80:83]
	v_mfma_f32_16x16x128_f8f6f4 v[72:75], v[16:23], v[222:229], v[72:75]
	v_mfma_f32_16x16x128_f8f6f4 v[64:67], v[24:31], v[230:237], v[64:67]
	v_mfma_f32_16x16x128_f8f6f4 v[56:59], v[16:23], v[230:237], v[56:59]
	v_mfma_f32_16x16x128_f8f6f4 v[48:51], v[24:31], v[238:245], v[48:51]
	v_mfma_f32_16x16x128_f8f6f4 v[40:43], v[16:23], v[238:245], v[40:43]
	v_mfma_f32_16x16x128_f8f6f4 v[84:87], v[8:15], v[214:221], v[84:87]
	v_mfma_f32_16x16x128_f8f6f4 v[76:79], v[0:7], v[214:221], v[76:79]
	v_mfma_f32_16x16x128_f8f6f4 v[68:71], v[8:15], v[222:229], v[68:71]
	v_mfma_f32_16x16x128_f8f6f4 v[60:63], v[0:7], v[222:229], v[60:63]
	v_mfma_f32_16x16x128_f8f6f4 v[52:55], v[8:15], v[230:237], v[52:55]
	v_mfma_f32_16x16x128_f8f6f4 v[44:47], v[0:7], v[230:237], v[44:47]
	v_mfma_f32_16x16x128_f8f6f4 v[36:39], v[8:15], v[238:245], v[36:39]
	v_mfma_f32_16x16x128_f8f6f4 v[32:35], v[0:7], v[238:245], v[32:35]
	s_setprio 0
	s_barrier
	s_add_i32 s30, 0, 0x18000
	s_add_i32 s31, 0, 0x1c000
	ds_read_b128 v[0:3], v252 offset:32768
	ds_read_b128 v[4:7], v253 offset:32768
	ds_read_b128 v[8:11], v252 offset:34816
	ds_read_b128 v[12:15], v253 offset:34816
	ds_read_b128 v[16:19], v252 offset:49152
	ds_read_b128 v[20:23], v253 offset:49152
	ds_read_b128 v[24:27], v252 offset:51200
	ds_read_b128 v[28:31], v253 offset:51200
	s_mov_b32 m0, s39
	v_lshl_add_u64 v[184:185], s[28:29], 0, v[184:185]
	ds_read_b128 v[214:217], v206 offset:32768
	ds_read_b128 v[222:225], v206 offset:34816
	ds_read_b128 v[218:221], v207 offset:32768
	ds_read_b128 v[226:229], v207 offset:34816
	ds_read_b128 v[230:233], v206 offset:36864
	ds_read_b128 v[238:241], v206 offset:38912
	ds_read_b128 v[234:237], v207 offset:36864
	ds_read_b128 v[242:245], v207 offset:38912
	global_load_lds_dwordx4 v[184:185], off
	v_lshl_add_u64 v[182:183], s[28:29], 0, v[182:183]
	s_mov_b32 m0, s40
	s_nop 0
	global_load_lds_dwordx4 v[182:183], off
	s_waitcnt vmcnt(8)
	s_waitcnt lgkmcnt(0)
	s_barrier
	s_setprio 1
	s_waitcnt lgkmcnt(0)
	v_mfma_f32_16x16x128_f8f6f4 v[156:159], v[0:7], v[214:221], v[156:159]
	v_mfma_f32_16x16x128_f8f6f4 v[152:155], v[8:15], v[214:221], v[152:155]
	v_mfma_f32_16x16x128_f8f6f4 v[144:147], v[0:7], v[222:229], v[144:147]
	v_mfma_f32_16x16x128_f8f6f4 v[136:139], v[8:15], v[222:229], v[136:139]
	v_mfma_f32_16x16x128_f8f6f4 v[128:131], v[0:7], v[230:237], v[128:131]
	v_mfma_f32_16x16x128_f8f6f4 v[120:123], v[8:15], v[230:237], v[120:123]
	v_mfma_f32_16x16x128_f8f6f4 v[112:115], v[0:7], v[238:245], v[112:115]
	v_mfma_f32_16x16x128_f8f6f4 v[104:107], v[8:15], v[238:245], v[104:107]
	v_mfma_f32_16x16x128_f8f6f4 v[148:151], v[16:23], v[214:221], v[148:151]
	v_mfma_f32_16x16x128_f8f6f4 v[140:143], v[24:31], v[214:221], v[140:143]
	v_mfma_f32_16x16x128_f8f6f4 v[132:135], v[16:23], v[222:229], v[132:135]
	v_mfma_f32_16x16x128_f8f6f4 v[124:127], v[24:31], v[222:229], v[124:127]
	v_mfma_f32_16x16x128_f8f6f4 v[116:119], v[16:23], v[230:237], v[116:119]
	v_mfma_f32_16x16x128_f8f6f4 v[108:111], v[24:31], v[230:237], v[108:111]
	v_mfma_f32_16x16x128_f8f6f4 v[100:103], v[16:23], v[238:245], v[100:103]
	v_mfma_f32_16x16x128_f8f6f4 v[96:99], v[24:31], v[238:245], v[96:99]
	s_setprio 0
	s_barrier
	s_add_i32 s28, s30, s36
	v_lshl_add_u64 v[182:183], v[186:187], 0, s[14:15]
	s_mov_b32 m0, s28
	ds_read_b128 v[214:217], v206 offset:49152
	ds_read_b128 v[222:225], v206 offset:51200
	ds_read_b128 v[218:221], v207 offset:49152
	ds_read_b128 v[226:229], v207 offset:51200
	ds_read_b128 v[230:233], v206 offset:53248
	ds_read_b128 v[238:241], v206 offset:55296
	ds_read_b128 v[234:237], v207 offset:53248
	ds_read_b128 v[242:245], v207 offset:55296
	global_load_lds_dwordx4 v[182:183], off
	v_lshl_add_u64 v[182:183], v[188:189], 0, s[14:15]
	s_add_i32 m0, s28, 0x2000
	s_add_i32 s28, s31, s36
	global_load_lds_dwordx4 v[182:183], off
	v_lshl_add_u64 v[182:183], v[190:191], 0, s[14:15]
	s_mov_b32 m0, s28
	s_nop 0
	global_load_lds_dwordx4 v[182:183], off
	v_lshl_add_u64 v[182:183], v[192:193], 0, s[14:15]
	s_add_i32 m0, s28, 0x2000
	s_nop 0
	global_load_lds_dwordx4 v[182:183], off
	v_lshl_add_u64 v[182:183], v[196:197], 0, s[14:15]
	s_mov_b32 m0, s41
	s_nop 0
	global_load_lds_dwordx4 v[182:183], off
	v_lshl_add_u64 v[182:183], v[194:195], 0, s[14:15]
	s_mov_b32 m0, s42
	s_nop 0
	global_load_lds_dwordx4 v[182:183], off
	s_waitcnt vmcnt(8)
	s_waitcnt lgkmcnt(0)
	s_barrier
	s_setprio 1
	s_waitcnt lgkmcnt(0)
	v_mfma_f32_16x16x128_f8f6f4 v[92:95], v[0:7], v[214:221], v[92:95]
	v_mfma_f32_16x16x128_f8f6f4 v[88:91], v[8:15], v[214:221], v[88:91]
	v_mfma_f32_16x16x128_f8f6f4 v[80:83], v[0:7], v[222:229], v[80:83]
	v_mfma_f32_16x16x128_f8f6f4 v[72:75], v[8:15], v[222:229], v[72:75]
	v_mfma_f32_16x16x128_f8f6f4 v[64:67], v[0:7], v[230:237], v[64:67]
	v_mfma_f32_16x16x128_f8f6f4 v[56:59], v[8:15], v[230:237], v[56:59]
	v_mfma_f32_16x16x128_f8f6f4 v[48:51], v[0:7], v[238:245], v[48:51]
	v_mfma_f32_16x16x128_f8f6f4 v[40:43], v[8:15], v[238:245], v[40:43]
	v_mfma_f32_16x16x128_f8f6f4 v[84:87], v[16:23], v[214:221], v[84:87]
	v_mfma_f32_16x16x128_f8f6f4 v[76:79], v[24:31], v[214:221], v[76:79]
	v_mfma_f32_16x16x128_f8f6f4 v[68:71], v[16:23], v[222:229], v[68:71]
	v_mfma_f32_16x16x128_f8f6f4 v[60:63], v[24:31], v[222:229], v[60:63]
	v_mfma_f32_16x16x128_f8f6f4 v[52:55], v[16:23], v[230:237], v[52:55]
	v_mfma_f32_16x16x128_f8f6f4 v[44:47], v[24:31], v[230:237], v[44:47]
	v_mfma_f32_16x16x128_f8f6f4 v[36:39], v[16:23], v[238:245], v[36:39]
	v_mfma_f32_16x16x128_f8f6f4 v[32:35], v[24:31], v[238:245], v[32:35]
	s_setprio 0
	s_barrier
	s_add_i32 s60, s60, 2
	s_add_u32 s26, s26, 0x100
	s_addc_u32 s27, s27, 0
	s_cmp_gt_u32 s60, 5
	s_cbranch_scc1 .LBB0_180

.LBB0_429:
	s_add_u32 s60, s24, 0x100
	s_addc_u32 s61, s25, 0
	v_mov_b32_e32 v101, v151
	v_mov_b32_e32 v105, v151
	s_add_u32 s62, s26, 0x100
	v_mov_b32_e32 v0, 0
	v_mov_b32_e32 v117, v151
	v_mov_b32_e32 v119, v151
	v_lshl_add_u64 v[154:155], s[16:17], 0, v[104:105]
	v_lshl_add_u64 v[156:157], s[16:17], 0, v[100:101]
	s_addc_u32 s63, s27, 0
	s_mov_b32 s64, -2
	s_mov_b64 s[24:25], 0
	v_mov_b32_e32 v1, v0
	v_mov_b32_e32 v2, v0
	v_mov_b32_e32 v3, v0
	v_mov_b32_e32 v4, v0
	v_mov_b32_e32 v5, v0
	v_mov_b32_e32 v6, v0
	v_mov_b32_e32 v7, v0
	v_mov_b32_e32 v16, v0
	v_mov_b32_e32 v17, v0
	v_mov_b32_e32 v18, v0
	v_mov_b32_e32 v19, v0
	v_mov_b32_e32 v20, v0
	v_mov_b32_e32 v21, v0
	v_mov_b32_e32 v22, v0
	v_mov_b32_e32 v23, v0
	v_mov_b32_e32 v32, v0
	v_mov_b32_e32 v33, v0
	v_mov_b32_e32 v34, v0
	v_mov_b32_e32 v35, v0
	v_mov_b32_e32 v36, v0
	v_mov_b32_e32 v37, v0
	v_mov_b32_e32 v38, v0
	v_mov_b32_e32 v39, v0
	v_mov_b32_e32 v48, v0
	v_mov_b32_e32 v49, v0
	v_mov_b32_e32 v50, v0
	v_mov_b32_e32 v51, v0
	v_mov_b32_e32 v52, v0
	v_mov_b32_e32 v53, v0
	v_mov_b32_e32 v54, v0
	v_mov_b32_e32 v55, v0
	v_mov_b32_e32 v8, v0
	v_mov_b32_e32 v9, v0
	v_mov_b32_e32 v10, v0
	v_mov_b32_e32 v11, v0
	v_mov_b32_e32 v12, v0
	v_mov_b32_e32 v13, v0
	v_mov_b32_e32 v14, v0
	v_mov_b32_e32 v15, v0
	v_mov_b32_e32 v24, v0
	v_mov_b32_e32 v25, v0
	v_mov_b32_e32 v26, v0
	v_mov_b32_e32 v27, v0
	v_mov_b32_e32 v28, v0
	v_mov_b32_e32 v29, v0
	v_mov_b32_e32 v30, v0
	v_mov_b32_e32 v31, v0
	v_mov_b32_e32 v40, v0
	v_mov_b32_e32 v41, v0
	v_mov_b32_e32 v42, v0
	v_mov_b32_e32 v43, v0
	v_mov_b32_e32 v44, v0
	v_mov_b32_e32 v45, v0
	v_mov_b32_e32 v46, v0
	v_mov_b32_e32 v47, v0
	v_mov_b32_e32 v56, v0
	v_mov_b32_e32 v57, v0
	v_mov_b32_e32 v58, v0
	v_mov_b32_e32 v59, v0
	v_mov_b32_e32 v60, v0
	v_mov_b32_e32 v61, v0
	v_mov_b32_e32 v62, v0
	v_mov_b32_e32 v63, v0
	v_mov_b32_e32 v64, v0
	v_mov_b32_e32 v65, v0
	v_mov_b32_e32 v66, v0
	v_mov_b32_e32 v67, v0
	v_mov_b32_e32 v68, v0
	v_mov_b32_e32 v69, v0
	v_mov_b32_e32 v70, v0
	v_mov_b32_e32 v71, v0
	v_mov_b32_e32 v80, v0
	v_mov_b32_e32 v81, v0
	v_mov_b32_e32 v82, v0
	v_mov_b32_e32 v83, v0
	v_mov_b32_e32 v84, v0
	v_mov_b32_e32 v85, v0
	v_mov_b32_e32 v86, v0
	v_mov_b32_e32 v87, v0
	v_mov_b32_e32 v96, v0
	v_mov_b32_e32 v97, v0
	v_mov_b32_e32 v98, v0
	v_mov_b32_e32 v99, v0
	v_mov_b32_e32 v108, v0
	v_mov_b32_e32 v109, v0
	v_mov_b32_e32 v110, v0
	v_mov_b32_e32 v111, v0
	v_mov_b32_e32 v128, v0
	v_mov_b32_e32 v129, v0
	v_mov_b32_e32 v130, v0
	v_mov_b32_e32 v131, v0
	v_mov_b32_e32 v132, v0
	v_mov_b32_e32 v133, v0
	v_mov_b32_e32 v134, v0
	v_mov_b32_e32 v135, v0
	v_mov_b32_e32 v72, v0
	v_mov_b32_e32 v73, v0
	v_mov_b32_e32 v74, v0
	v_mov_b32_e32 v75, v0
	v_mov_b32_e32 v76, v0
	v_mov_b32_e32 v77, v0
	v_mov_b32_e32 v78, v0
	v_mov_b32_e32 v79, v0
	v_mov_b32_e32 v88, v0
	v_mov_b32_e32 v89, v0
	v_mov_b32_e32 v90, v0
	v_mov_b32_e32 v91, v0
	v_mov_b32_e32 v92, v0
	v_mov_b32_e32 v93, v0
	v_mov_b32_e32 v94, v0
	v_mov_b32_e32 v95, v0
	v_mov_b32_e32 v120, v0
	v_mov_b32_e32 v121, v0
	v_mov_b32_e32 v122, v0
	v_mov_b32_e32 v123, v0
	v_mov_b32_e32 v124, v0
	v_mov_b32_e32 v125, v0
	v_mov_b32_e32 v126, v0
	v_mov_b32_e32 v127, v0
	v_mov_b32_e32 v136, v0
	v_mov_b32_e32 v137, v0
	v_mov_b32_e32 v138, v0
	v_mov_b32_e32 v139, v0
	v_mov_b32_e32 v140, v0
	v_mov_b32_e32 v141, v0
	v_mov_b32_e32 v142, v0
	v_mov_b32_e32 v143, v0
	v_add_u32_e32 v252, 0x10000, v167
	v_add_u32_e32 v253, 0x10000, v168
	s_branch .LBB0_431
.LBB0_430:
	s_add_u32 s26, s4, s24
	s_addc_u32 s27, s5, s25
	s_add_u32 s30, s26, 0x21c00100
	s_addc_u32 s31, s27, 0
	ds_read_b128 v[172:175], v252
	ds_read_b128 v[176:179], v253
	s_and_b64 s[26:27], s[28:29], exec
	ds_read_b128 v[180:183], v252 offset:2048
	ds_read_b128 v[184:187], v253 offset:2048
	s_cselect_b32 s27, s7, s31
	s_cselect_b32 s26, s6, s30
	s_add_u32 s65, s60, s24
	ds_read_b128 v[188:191], v252 offset:16384
	ds_read_b128 v[192:195], v253 offset:16384
	s_addc_u32 s66, s61, s25
	ds_read_b128 v[196:199], v252 offset:18432
	ds_read_b128 v[200:203], v253 offset:18432
	s_and_b64 s[30:31], s[28:29], exec
	s_cselect_b32 s31, s21, s66
	s_cselect_b32 s30, s20, s65
	s_add_u32 s65, s62, s24
	s_addc_u32 s66, s63, s25
	s_and_b64 s[28:29], s[28:29], exec
	s_cselect_b32 s29, s23, s66
	s_cselect_b32 s28, s22, s65
	v_lshl_add_u64 v[236:237], v[156:157], 0, s[24:25]
	s_add_i32 m0, s37, 0xc000
	ds_read_b128 v[204:207], v169
	ds_read_b128 v[208:211], v169 offset:1024
	ds_read_b128 v[212:215], v169 offset:2048
	ds_read_b128 v[216:219], v169 offset:3072
	ds_read_b128 v[220:223], v169 offset:4096
	ds_read_b128 v[224:227], v169 offset:5120
	ds_read_b128 v[228:231], v169 offset:6144
	ds_read_b128 v[232:235], v169 offset:7168
	global_load_lds_dwordx4 v[236:237], off
	v_lshl_add_u64 v[236:237], v[154:155], 0, s[24:25]
	s_add_i32 m0, s37, 0xe000
	s_nop 0
	global_load_lds_dwordx4 v[236:237], off
	s_waitcnt vmcnt(8)
	s_waitcnt lgkmcnt(0)
	s_barrier
	s_setprio 1
	s_waitcnt lgkmcnt(0)
	v_mfma_f32_16x16x32_bf16 v[140:143], v[172:175], v[204:207], v[140:143]
	v_mfma_f32_16x16x32_bf16 v[136:139], v[180:183], v[204:207], v[136:139]
	v_mfma_f32_16x16x32_bf16 v[124:127], v[172:175], v[212:215], v[124:127]
	v_mfma_f32_16x16x32_bf16 v[120:123], v[180:183], v[212:215], v[120:123]
	v_mfma_f32_16x16x32_bf16 v[92:95], v[172:175], v[220:223], v[92:95]
	v_mfma_f32_16x16x32_bf16 v[88:91], v[180:183], v[220:223], v[88:91]
	v_mfma_f32_16x16x32_bf16 v[76:79], v[172:175], v[228:231], v[76:79]
	v_mfma_f32_16x16x32_bf16 v[72:75], v[180:183], v[228:231], v[72:75]
	v_mfma_f32_16x16x32_bf16 v[140:143], v[176:179], v[208:211], v[140:143]
	v_mfma_f32_16x16x32_bf16 v[136:139], v[184:187], v[208:211], v[136:139]
	v_mfma_f32_16x16x32_bf16 v[124:127], v[176:179], v[216:219], v[124:127]
	v_mfma_f32_16x16x32_bf16 v[120:123], v[184:187], v[216:219], v[120:123]
	v_mfma_f32_16x16x32_bf16 v[92:95], v[176:179], v[224:227], v[92:95]
	v_mfma_f32_16x16x32_bf16 v[88:91], v[184:187], v[224:227], v[88:91]
	v_mfma_f32_16x16x32_bf16 v[76:79], v[176:179], v[232:235], v[76:79]
	v_mfma_f32_16x16x32_bf16 v[72:75], v[184:187], v[232:235], v[72:75]
	v_mfma_f32_16x16x32_bf16 v[132:135], v[188:191], v[204:207], v[132:135]
	v_mfma_f32_16x16x32_bf16 v[128:131], v[196:199], v[204:207], v[128:131]
	v_mfma_f32_16x16x32_bf16 v[108:111], v[188:191], v[212:215], v[108:111]
	v_mfma_f32_16x16x32_bf16 v[96:99], v[196:199], v[212:215], v[96:99]
	v_mfma_f32_16x16x32_bf16 v[84:87], v[188:191], v[220:223], v[84:87]
	v_mfma_f32_16x16x32_bf16 v[80:83], v[196:199], v[220:223], v[80:83]
	v_mfma_f32_16x16x32_bf16 v[68:71], v[188:191], v[228:231], v[68:71]
	v_mfma_f32_16x16x32_bf16 v[64:67], v[196:199], v[228:231], v[64:67]
	v_mfma_f32_16x16x32_bf16 v[132:135], v[192:195], v[208:211], v[132:135]
	v_mfma_f32_16x16x32_bf16 v[128:131], v[200:203], v[208:211], v[128:131]
	v_mfma_f32_16x16x32_bf16 v[108:111], v[192:195], v[216:219], v[108:111]
	v_mfma_f32_16x16x32_bf16 v[96:99], v[200:203], v[216:219], v[96:99]
	v_mfma_f32_16x16x32_bf16 v[84:87], v[192:195], v[224:227], v[84:87]
	v_mfma_f32_16x16x32_bf16 v[80:83], v[200:203], v[224:227], v[80:83]
	v_mfma_f32_16x16x32_bf16 v[68:71], v[192:195], v[232:235], v[68:71]
	v_mfma_f32_16x16x32_bf16 v[64:67], v[200:203], v[232:235], v[64:67]
	s_setprio 0
	s_barrier
	s_add_i32 s65, s48, s35
	v_lshl_add_u64 v[236:237], s[30:31], 0, v[146:147]
	s_mov_b32 m0, s65
	ds_read_b128 v[204:207], v169 offset:16384
	ds_read_b128 v[208:211], v169 offset:17408
	ds_read_b128 v[212:215], v169 offset:18432
	ds_read_b128 v[216:219], v169 offset:19456
	ds_read_b128 v[220:223], v169 offset:20480
	ds_read_b128 v[224:227], v169 offset:21504
	ds_read_b128 v[228:231], v169 offset:22528
	ds_read_b128 v[232:235], v169 offset:23552
	global_load_lds_dwordx4 v[236:237], off
	v_lshl_add_u64 v[238:239], s[30:31], 0, v[148:149]
	s_add_i32 m0, s65, 0x2000
	s_add_i32 s30, s50, s35
	global_load_lds_dwordx4 v[238:239], off
	v_lshl_add_u64 v[240:241], s[28:29], 0, v[146:147]
	s_mov_b32 m0, s30
	v_lshl_add_u64 v[242:243], s[28:29], 0, v[148:149]
	global_load_lds_dwordx4 v[240:241], off
	s_add_i32 m0, s30, 0x2000
	v_mov_b32_e32 v153, v151
	global_load_lds_dwordx4 v[242:243], off
	s_mov_b32 m0, s37
	v_lshl_add_u64 v[244:245], s[26:27], 0, v[150:151]
	global_load_lds_dwordx4 v150, s[26:27]
	s_mov_b32 m0, s38
	v_lshl_add_u64 v[246:247], s[26:27], 0, v[152:153]
	global_load_lds_dwordx4 v152, s[26:27]
	s_waitcnt vmcnt(8)
	s_waitcnt lgkmcnt(0)
	s_barrier
	s_setprio 1
	s_waitcnt lgkmcnt(0)
	v_mfma_f32_16x16x32_bf16 v[60:63], v[172:175], v[204:207], v[60:63]
	v_mfma_f32_16x16x32_bf16 v[56:59], v[180:183], v[204:207], v[56:59]
	v_mfma_f32_16x16x32_bf16 v[44:47], v[172:175], v[212:215], v[44:47]
	v_mfma_f32_16x16x32_bf16 v[40:43], v[180:183], v[212:215], v[40:43]
	v_mfma_f32_16x16x32_bf16 v[28:31], v[172:175], v[220:223], v[28:31]
	v_mfma_f32_16x16x32_bf16 v[24:27], v[180:183], v[220:223], v[24:27]
	v_mfma_f32_16x16x32_bf16 v[12:15], v[172:175], v[228:231], v[12:15]
	v_mfma_f32_16x16x32_bf16 v[8:11], v[180:183], v[228:231], v[8:11]
	v_mfma_f32_16x16x32_bf16 v[60:63], v[176:179], v[208:211], v[60:63]
	v_mfma_f32_16x16x32_bf16 v[56:59], v[184:187], v[208:211], v[56:59]
	v_mfma_f32_16x16x32_bf16 v[44:47], v[176:179], v[216:219], v[44:47]
	v_mfma_f32_16x16x32_bf16 v[40:43], v[184:187], v[216:219], v[40:43]
	v_mfma_f32_16x16x32_bf16 v[28:31], v[176:179], v[224:227], v[28:31]
	v_mfma_f32_16x16x32_bf16 v[24:27], v[184:187], v[224:227], v[24:27]
	v_mfma_f32_16x16x32_bf16 v[12:15], v[176:179], v[232:235], v[12:15]
	v_mfma_f32_16x16x32_bf16 v[8:11], v[184:187], v[232:235], v[8:11]
	v_mfma_f32_16x16x32_bf16 v[52:55], v[188:191], v[204:207], v[52:55]
	v_mfma_f32_16x16x32_bf16 v[48:51], v[196:199], v[204:207], v[48:51]
	v_mfma_f32_16x16x32_bf16 v[36:39], v[188:191], v[212:215], v[36:39]
	v_mfma_f32_16x16x32_bf16 v[32:35], v[196:199], v[212:215], v[32:35]
	v_mfma_f32_16x16x32_bf16 v[20:23], v[188:191], v[220:223], v[20:23]
	v_mfma_f32_16x16x32_bf16 v[16:19], v[196:199], v[220:223], v[16:19]
	v_mfma_f32_16x16x32_bf16 v[4:7], v[188:191], v[228:231], v[4:7]
	v_mfma_f32_16x16x32_bf16 v[0:3], v[196:199], v[228:231], v[0:3]
	v_mfma_f32_16x16x32_bf16 v[52:55], v[192:195], v[208:211], v[52:55]
	v_mfma_f32_16x16x32_bf16 v[48:51], v[200:203], v[208:211], v[48:51]
	v_mfma_f32_16x16x32_bf16 v[36:39], v[192:195], v[216:219], v[36:39]
	v_mfma_f32_16x16x32_bf16 v[32:35], v[200:203], v[216:219], v[32:35]
	v_mfma_f32_16x16x32_bf16 v[20:23], v[192:195], v[224:227], v[20:23]
	v_mfma_f32_16x16x32_bf16 v[16:19], v[200:203], v[224:227], v[16:19]
	v_mfma_f32_16x16x32_bf16 v[4:7], v[192:195], v[232:235], v[4:7]
	v_mfma_f32_16x16x32_bf16 v[0:3], v[200:203], v[232:235], v[0:3]
	s_setprio 0
	s_barrier
	s_add_i32 s28, 0, 0x18000
	ds_read_b128 v[172:175], v252 offset:32768
	ds_read_b128 v[176:179], v253 offset:32768
	s_add_i32 s29, 0, 0x1c000
	ds_read_b128 v[180:183], v252 offset:34816
	ds_read_b128 v[184:187], v253 offset:34816
	ds_read_b128 v[188:191], v252 offset:49152
	ds_read_b128 v[192:195], v253 offset:49152
	ds_read_b128 v[196:199], v252 offset:51200
	ds_read_b128 v[200:203], v253 offset:51200
	s_mov_b32 m0, s39
	v_lshl_add_u64 v[160:161], s[26:27], 0, v[160:161]
	ds_read_b128 v[204:207], v169 offset:32768
	ds_read_b128 v[208:211], v169 offset:33792
	ds_read_b128 v[212:215], v169 offset:34816
	ds_read_b128 v[216:219], v169 offset:35840
	ds_read_b128 v[220:223], v169 offset:36864
	ds_read_b128 v[224:227], v169 offset:37888
	ds_read_b128 v[228:231], v169 offset:38912
	ds_read_b128 v[232:235], v169 offset:39936
	global_load_lds_dwordx4 v[160:161], off
	v_lshl_add_u64 v[158:159], s[26:27], 0, v[158:159]
	s_mov_b32 m0, s40
	s_nop 0
	global_load_lds_dwordx4 v[158:159], off
	s_waitcnt vmcnt(8)
	s_waitcnt lgkmcnt(0)
	s_barrier
	s_setprio 1
	s_waitcnt lgkmcnt(0)
	v_mfma_f32_16x16x32_bf16 v[140:143], v[172:175], v[204:207], v[140:143]
	v_mfma_f32_16x16x32_bf16 v[136:139], v[180:183], v[204:207], v[136:139]
	v_mfma_f32_16x16x32_bf16 v[124:127], v[172:175], v[212:215], v[124:127]
	v_mfma_f32_16x16x32_bf16 v[120:123], v[180:183], v[212:215], v[120:123]
	v_mfma_f32_16x16x32_bf16 v[92:95], v[172:175], v[220:223], v[92:95]
	v_mfma_f32_16x16x32_bf16 v[88:91], v[180:183], v[220:223], v[88:91]
	v_mfma_f32_16x16x32_bf16 v[76:79], v[172:175], v[228:231], v[76:79]
	v_mfma_f32_16x16x32_bf16 v[72:75], v[180:183], v[228:231], v[72:75]
	v_mfma_f32_16x16x32_bf16 v[140:143], v[176:179], v[208:211], v[140:143]
	v_mfma_f32_16x16x32_bf16 v[136:139], v[184:187], v[208:211], v[136:139]
	v_mfma_f32_16x16x32_bf16 v[124:127], v[176:179], v[216:219], v[124:127]
	v_mfma_f32_16x16x32_bf16 v[120:123], v[184:187], v[216:219], v[120:123]
	v_mfma_f32_16x16x32_bf16 v[92:95], v[176:179], v[224:227], v[92:95]
	v_mfma_f32_16x16x32_bf16 v[88:91], v[184:187], v[224:227], v[88:91]
	v_mfma_f32_16x16x32_bf16 v[76:79], v[176:179], v[232:235], v[76:79]
	v_mfma_f32_16x16x32_bf16 v[72:75], v[184:187], v[232:235], v[72:75]
	v_mfma_f32_16x16x32_bf16 v[132:135], v[188:191], v[204:207], v[132:135]
	v_mfma_f32_16x16x32_bf16 v[128:131], v[196:199], v[204:207], v[128:131]
	v_mfma_f32_16x16x32_bf16 v[108:111], v[188:191], v[212:215], v[108:111]
	v_mfma_f32_16x16x32_bf16 v[96:99], v[196:199], v[212:215], v[96:99]
	v_mfma_f32_16x16x32_bf16 v[84:87], v[188:191], v[220:223], v[84:87]
	v_mfma_f32_16x16x32_bf16 v[80:83], v[196:199], v[220:223], v[80:83]
	v_mfma_f32_16x16x32_bf16 v[68:71], v[188:191], v[228:231], v[68:71]
	v_mfma_f32_16x16x32_bf16 v[64:67], v[196:199], v[228:231], v[64:67]
	v_mfma_f32_16x16x32_bf16 v[132:135], v[192:195], v[208:211], v[132:135]
	v_mfma_f32_16x16x32_bf16 v[128:131], v[200:203], v[208:211], v[128:131]
	v_mfma_f32_16x16x32_bf16 v[108:111], v[192:195], v[216:219], v[108:111]
	v_mfma_f32_16x16x32_bf16 v[96:99], v[200:203], v[216:219], v[96:99]
	v_mfma_f32_16x16x32_bf16 v[84:87], v[192:195], v[224:227], v[84:87]
	v_mfma_f32_16x16x32_bf16 v[80:83], v[200:203], v[224:227], v[80:83]
	v_mfma_f32_16x16x32_bf16 v[68:71], v[192:195], v[232:235], v[68:71]
	v_mfma_f32_16x16x32_bf16 v[64:67], v[200:203], v[232:235], v[64:67]
	s_setprio 0
	s_barrier
	s_add_i32 s26, s28, s35
	v_lshl_add_u64 v[232:233], v[236:237], 0, s[14:15]
	s_mov_b32 m0, s26
	ds_read_b128 v[158:161], v169 offset:49152
	ds_read_b128 v[204:207], v169 offset:50176
	ds_read_b128 v[208:211], v169 offset:51200
	ds_read_b128 v[212:215], v169 offset:52224
	ds_read_b128 v[216:219], v169 offset:53248
	ds_read_b128 v[220:223], v169 offset:54272
	ds_read_b128 v[224:227], v169 offset:55296
	ds_read_b128 v[228:231], v169 offset:56320
	global_load_lds_dwordx4 v[232:233], off
	v_lshl_add_u64 v[232:233], v[238:239], 0, s[14:15]
	s_add_i32 m0, s26, 0x2000
	s_add_i32 s26, s29, s35
	global_load_lds_dwordx4 v[232:233], off
	v_lshl_add_u64 v[232:233], v[240:241], 0, s[14:15]
	s_mov_b32 m0, s26
	s_nop 0
	global_load_lds_dwordx4 v[232:233], off
	v_lshl_add_u64 v[232:233], v[242:243], 0, s[14:15]
	s_add_i32 m0, s26, 0x2000
	s_nop 0
	global_load_lds_dwordx4 v[232:233], off
	v_lshl_add_u64 v[232:233], v[244:245], 0, s[14:15]
	s_mov_b32 m0, s45
	s_nop 0
	global_load_lds_dwordx4 v[232:233], off
	v_lshl_add_u64 v[232:233], v[246:247], 0, s[14:15]
	s_mov_b32 m0, s46
	s_nop 0
	global_load_lds_dwordx4 v[232:233], off
	s_waitcnt vmcnt(8)
	s_waitcnt lgkmcnt(0)
	s_barrier
	s_setprio 1
	s_waitcnt lgkmcnt(0)
	v_mfma_f32_16x16x32_bf16 v[60:63], v[172:175], v[158:161], v[60:63]
	v_mfma_f32_16x16x32_bf16 v[56:59], v[180:183], v[158:161], v[56:59]
	v_mfma_f32_16x16x32_bf16 v[44:47], v[172:175], v[208:211], v[44:47]
	v_mfma_f32_16x16x32_bf16 v[40:43], v[180:183], v[208:211], v[40:43]
	v_mfma_f32_16x16x32_bf16 v[28:31], v[172:175], v[216:219], v[28:31]
	v_mfma_f32_16x16x32_bf16 v[24:27], v[180:183], v[216:219], v[24:27]
	v_mfma_f32_16x16x32_bf16 v[12:15], v[172:175], v[224:227], v[12:15]
	v_mfma_f32_16x16x32_bf16 v[8:11], v[180:183], v[224:227], v[8:11]
	v_mfma_f32_16x16x32_bf16 v[60:63], v[176:179], v[204:207], v[60:63]
	v_mfma_f32_16x16x32_bf16 v[56:59], v[184:187], v[204:207], v[56:59]
	v_mfma_f32_16x16x32_bf16 v[44:47], v[176:179], v[212:215], v[44:47]
	v_mfma_f32_16x16x32_bf16 v[40:43], v[184:187], v[212:215], v[40:43]
	v_mfma_f32_16x16x32_bf16 v[28:31], v[176:179], v[220:223], v[28:31]
	v_mfma_f32_16x16x32_bf16 v[24:27], v[184:187], v[220:223], v[24:27]
	v_mfma_f32_16x16x32_bf16 v[12:15], v[176:179], v[228:231], v[12:15]
	v_mfma_f32_16x16x32_bf16 v[8:11], v[184:187], v[228:231], v[8:11]
	v_mfma_f32_16x16x32_bf16 v[52:55], v[188:191], v[158:161], v[52:55]
	v_mfma_f32_16x16x32_bf16 v[48:51], v[196:199], v[158:161], v[48:51]
	v_mfma_f32_16x16x32_bf16 v[36:39], v[188:191], v[208:211], v[36:39]
	v_mfma_f32_16x16x32_bf16 v[32:35], v[196:199], v[208:211], v[32:35]
	v_mfma_f32_16x16x32_bf16 v[20:23], v[188:191], v[216:219], v[20:23]
	v_mfma_f32_16x16x32_bf16 v[16:19], v[196:199], v[216:219], v[16:19]
	v_mfma_f32_16x16x32_bf16 v[4:7], v[188:191], v[224:227], v[4:7]
	v_mfma_f32_16x16x32_bf16 v[0:3], v[196:199], v[224:227], v[0:3]
	v_mfma_f32_16x16x32_bf16 v[52:55], v[192:195], v[204:207], v[52:55]
	v_mfma_f32_16x16x32_bf16 v[48:51], v[200:203], v[204:207], v[48:51]
	v_mfma_f32_16x16x32_bf16 v[36:39], v[192:195], v[212:215], v[36:39]
	v_mfma_f32_16x16x32_bf16 v[32:35], v[200:203], v[212:215], v[32:35]
	v_mfma_f32_16x16x32_bf16 v[20:23], v[192:195], v[220:223], v[20:23]
	v_mfma_f32_16x16x32_bf16 v[16:19], v[200:203], v[220:223], v[16:19]
	v_mfma_f32_16x16x32_bf16 v[4:7], v[192:195], v[228:231], v[4:7]
	v_mfma_f32_16x16x32_bf16 v[0:3], v[200:203], v[228:231], v[0:3]
	s_setprio 0
	s_barrier
	s_add_i32 s64, s64, 2
	s_add_u32 s24, s24, 0x100
	s_addc_u32 s25, s25, 0
	s_cmp_gt_u32 s64, 9
	s_cbranch_scc1 .LBB0_433

.LBB0_589:
	s_lshl_b32 s4, s80, 10
	s_and_b32 s4, s4, 0x400
	s_add_u32 s27, s38, 0x100
	s_addc_u32 s86, s39, 0
	v_mov_b32_e32 v171, v165
	v_mov_b32_e32 v169, v165
	s_add_u32 s87, s40, 0x100
	v_mov_b32_e32 v32, 0
	v_add_u32_e32 v208, s4, v199
	v_lshl_add_u64 v[174:175], s[18:19], 0, v[168:169]
	v_lshl_add_u64 v[176:177], s[18:19], 0, v[170:171]
	s_addc_u32 s88, s41, 0
	s_mov_b32 s89, -2
	s_mov_b64 s[4:5], 0
	v_mov_b32_e32 v33, v32
	v_mov_b32_e32 v34, v32
	v_mov_b32_e32 v35, v32
	v_mov_b32_e32 v40, v32
	v_mov_b32_e32 v41, v32
	v_mov_b32_e32 v42, v32
	v_mov_b32_e32 v43, v32
	v_mov_b32_e32 v48, v32
	v_mov_b32_e32 v49, v32
	v_mov_b32_e32 v50, v32
	v_mov_b32_e32 v51, v32
	v_mov_b32_e32 v56, v32
	v_mov_b32_e32 v57, v32
	v_mov_b32_e32 v58, v32
	v_mov_b32_e32 v59, v32
	v_mov_b32_e32 v64, v32
	v_mov_b32_e32 v65, v32
	v_mov_b32_e32 v66, v32
	v_mov_b32_e32 v67, v32
	v_mov_b32_e32 v72, v32
	v_mov_b32_e32 v73, v32
	v_mov_b32_e32 v74, v32
	v_mov_b32_e32 v75, v32
	v_mov_b32_e32 v80, v32
	v_mov_b32_e32 v81, v32
	v_mov_b32_e32 v82, v32
	v_mov_b32_e32 v83, v32
	v_mov_b32_e32 v88, v32
	v_mov_b32_e32 v89, v32
	v_mov_b32_e32 v90, v32
	v_mov_b32_e32 v91, v32
	v_mov_b32_e32 v36, v32
	v_mov_b32_e32 v37, v32
	v_mov_b32_e32 v38, v32
	v_mov_b32_e32 v39, v32
	v_mov_b32_e32 v44, v32
	v_mov_b32_e32 v45, v32
	v_mov_b32_e32 v46, v32
	v_mov_b32_e32 v47, v32
	v_mov_b32_e32 v52, v32
	v_mov_b32_e32 v53, v32
	v_mov_b32_e32 v54, v32
	v_mov_b32_e32 v55, v32
	v_mov_b32_e32 v60, v32
	v_mov_b32_e32 v61, v32
	v_mov_b32_e32 v62, v32
	v_mov_b32_e32 v63, v32
	v_mov_b32_e32 v68, v32
	v_mov_b32_e32 v69, v32
	v_mov_b32_e32 v70, v32
	v_mov_b32_e32 v71, v32
	v_mov_b32_e32 v76, v32
	v_mov_b32_e32 v77, v32
	v_mov_b32_e32 v78, v32
	v_mov_b32_e32 v79, v32
	v_mov_b32_e32 v84, v32
	v_mov_b32_e32 v85, v32
	v_mov_b32_e32 v86, v32
	v_mov_b32_e32 v87, v32
	v_mov_b32_e32 v92, v32
	v_mov_b32_e32 v93, v32
	v_mov_b32_e32 v94, v32
	v_mov_b32_e32 v95, v32
	v_mov_b32_e32 v96, v32
	v_mov_b32_e32 v97, v32
	v_mov_b32_e32 v98, v32
	v_mov_b32_e32 v99, v32
	v_mov_b32_e32 v104, v32
	v_mov_b32_e32 v105, v32
	v_mov_b32_e32 v106, v32
	v_mov_b32_e32 v107, v32
	v_mov_b32_e32 v112, v32
	v_mov_b32_e32 v113, v32
	v_mov_b32_e32 v114, v32
	v_mov_b32_e32 v115, v32
	v_mov_b32_e32 v120, v32
	v_mov_b32_e32 v121, v32
	v_mov_b32_e32 v122, v32
	v_mov_b32_e32 v123, v32
	v_mov_b32_e32 v128, v32
	v_mov_b32_e32 v129, v32
	v_mov_b32_e32 v130, v32
	v_mov_b32_e32 v131, v32
	v_mov_b32_e32 v136, v32
	v_mov_b32_e32 v137, v32
	v_mov_b32_e32 v138, v32
	v_mov_b32_e32 v139, v32
	v_mov_b32_e32 v144, v32
	v_mov_b32_e32 v145, v32
	v_mov_b32_e32 v146, v32
	v_mov_b32_e32 v147, v32
	v_mov_b32_e32 v152, v32
	v_mov_b32_e32 v153, v32
	v_mov_b32_e32 v154, v32
	v_mov_b32_e32 v155, v32
	v_mov_b32_e32 v100, v32
	v_mov_b32_e32 v101, v32
	v_mov_b32_e32 v102, v32
	v_mov_b32_e32 v103, v32
	v_mov_b32_e32 v108, v32
	v_mov_b32_e32 v109, v32
	v_mov_b32_e32 v110, v32
	v_mov_b32_e32 v111, v32
	v_mov_b32_e32 v116, v32
	v_mov_b32_e32 v117, v32
	v_mov_b32_e32 v118, v32
	v_mov_b32_e32 v119, v32
	v_mov_b32_e32 v124, v32
	v_mov_b32_e32 v125, v32
	v_mov_b32_e32 v126, v32
	v_mov_b32_e32 v127, v32
	v_mov_b32_e32 v132, v32
	v_mov_b32_e32 v133, v32
	v_mov_b32_e32 v134, v32
	v_mov_b32_e32 v135, v32
	v_mov_b32_e32 v140, v32
	v_mov_b32_e32 v141, v32
	v_mov_b32_e32 v142, v32
	v_mov_b32_e32 v143, v32
	v_mov_b32_e32 v148, v32
	v_mov_b32_e32 v149, v32
	v_mov_b32_e32 v150, v32
	v_mov_b32_e32 v151, v32
	v_mov_b32_e32 v156, v32
	v_mov_b32_e32 v157, v32
	v_mov_b32_e32 v158, v32
	v_mov_b32_e32 v159, v32
	v_add_u32_e32 v252, 0x10000, v197
	v_add_u32_e32 v253, 0x10000, v198
	s_branch .LBB0_591
.LBB0_590:
	s_add_u32 s36, s8, s4
	s_addc_u32 s37, s9, s5
	s_add_u32 s38, s36, 0xe000100
	s_addc_u32 s39, s37, 0
	ds_read_b128 v[24:27], v252
	ds_read_b128 v[28:31], v253
	s_and_b64 s[36:37], s[40:41], exec
	ds_read_b128 v[16:19], v252 offset:2048
	ds_read_b128 v[20:23], v253 offset:2048
	s_cselect_b32 s37, s11, s39
	s_cselect_b32 s36, s10, s38
	s_add_u32 s90, s27, s4
	ds_read_b128 v[8:11], v252 offset:16384
	ds_read_b128 v[12:15], v253 offset:16384
	s_addc_u32 s91, s86, s5
	ds_read_b128 v[0:3], v252 offset:18432
	ds_read_b128 v[4:7], v253 offset:18432
	s_and_b64 s[38:39], s[40:41], exec
	s_cselect_b32 s39, s29, s91
	s_cselect_b32 s38, s28, s90
	s_add_u32 s90, s87, s4
	s_addc_u32 s91, s88, s5
	s_and_b64 s[40:41], s[40:41], exec
	s_cselect_b32 s41, s31, s91
	s_cselect_b32 s40, s30, s90
	v_lshl_add_u64 v[190:191], v[176:177], 0, s[4:5]
	s_add_i32 m0, s61, 0xc000
	ds_read_b128 v[182:185], v201
	ds_read_b128 v[210:213], v201 offset:2048
	ds_read_b128 v[186:189], v202
	ds_read_b128 v[214:217], v202 offset:2048
	ds_read_b128 v[218:221], v201 offset:4096
	ds_read_b128 v[226:229], v201 offset:6144
	ds_read_b128 v[222:225], v202 offset:4096
	ds_read_b128 v[230:233], v202 offset:6144
	global_load_lds_dwordx4 v[190:191], off
	v_lshl_add_u64 v[190:191], v[174:175], 0, s[4:5]
	s_add_i32 m0, s61, 0xe000
	s_nop 0
	global_load_lds_dwordx4 v[190:191], off
	s_waitcnt vmcnt(8)
	s_waitcnt lgkmcnt(0)
	s_barrier
	s_setprio 1
	s_waitcnt lgkmcnt(0)
	v_mfma_f32_16x16x128_f8f6f4 v[156:159], v[24:31], v[182:189], v[156:159]
	v_mfma_f32_16x16x128_f8f6f4 v[148:151], v[16:23], v[182:189], v[148:151]
	v_mfma_f32_16x16x128_f8f6f4 v[140:143], v[24:31], v[210:217], v[140:143]
	v_mfma_f32_16x16x128_f8f6f4 v[132:135], v[16:23], v[210:217], v[132:135]
	v_mfma_f32_16x16x128_f8f6f4 v[124:127], v[24:31], v[218:225], v[124:127]
	v_mfma_f32_16x16x128_f8f6f4 v[116:119], v[16:23], v[218:225], v[116:119]
	v_mfma_f32_16x16x128_f8f6f4 v[108:111], v[24:31], v[226:233], v[108:111]
	v_mfma_f32_16x16x128_f8f6f4 v[100:103], v[16:23], v[226:233], v[100:103]
	v_mfma_f32_16x16x128_f8f6f4 v[152:155], v[8:15], v[182:189], v[152:155]
	v_mfma_f32_16x16x128_f8f6f4 v[144:147], v[0:7], v[182:189], v[144:147]
	v_mfma_f32_16x16x128_f8f6f4 v[136:139], v[8:15], v[210:217], v[136:139]
	v_mfma_f32_16x16x128_f8f6f4 v[128:131], v[0:7], v[210:217], v[128:131]
	v_mfma_f32_16x16x128_f8f6f4 v[120:123], v[8:15], v[218:225], v[120:123]
	v_mfma_f32_16x16x128_f8f6f4 v[112:115], v[0:7], v[218:225], v[112:115]
	v_mfma_f32_16x16x128_f8f6f4 v[104:107], v[8:15], v[226:233], v[104:107]
	v_mfma_f32_16x16x128_f8f6f4 v[96:99], v[0:7], v[226:233], v[96:99]
	s_setprio 0
	s_barrier
	s_add_i32 s90, s72, s44
	v_lshl_add_u64 v[182:183], s[38:39], 0, v[160:161]
	s_mov_b32 m0, s90
	ds_read_b128 v[210:213], v201 offset:16384
	ds_read_b128 v[218:221], v201 offset:18432
	ds_read_b128 v[214:217], v202 offset:16384
	ds_read_b128 v[222:225], v202 offset:18432
	ds_read_b128 v[226:229], v201 offset:20480
	ds_read_b128 v[234:237], v201 offset:22528
	ds_read_b128 v[230:233], v202 offset:20480
	ds_read_b128 v[238:241], v202 offset:22528
	global_load_lds_dwordx4 v[182:183], off
	v_lshl_add_u64 v[184:185], s[38:39], 0, v[162:163]
	s_add_i32 m0, s90, 0x2000
	s_add_i32 s38, s74, s44
	global_load_lds_dwordx4 v[184:185], off
	v_lshl_add_u64 v[186:187], s[40:41], 0, v[160:161]
	s_mov_b32 m0, s38
	v_lshl_add_u64 v[188:189], s[40:41], 0, v[162:163]
	global_load_lds_dwordx4 v[186:187], off
	s_add_i32 m0, s38, 0x2000
	v_mov_b32_e32 v167, v165
	global_load_lds_dwordx4 v[188:189], off
	s_mov_b32 m0, s61
	v_lshl_add_u64 v[192:193], s[36:37], 0, v[164:165]
	global_load_lds_dwordx4 v164, s[36:37]
	s_mov_b32 m0, s62
	v_lshl_add_u64 v[190:191], s[36:37], 0, v[166:167]
	global_load_lds_dwordx4 v166, s[36:37]
	s_waitcnt vmcnt(8)
	s_waitcnt lgkmcnt(0)
	s_barrier
	s_setprio 1
	s_waitcnt lgkmcnt(0)
	v_mfma_f32_16x16x128_f8f6f4 v[92:95], v[24:31], v[210:217], v[92:95]
	v_mfma_f32_16x16x128_f8f6f4 v[84:87], v[16:23], v[210:217], v[84:87]
	v_mfma_f32_16x16x128_f8f6f4 v[76:79], v[24:31], v[218:225], v[76:79]
	v_mfma_f32_16x16x128_f8f6f4 v[68:71], v[16:23], v[218:225], v[68:71]
	v_mfma_f32_16x16x128_f8f6f4 v[60:63], v[24:31], v[226:233], v[60:63]
	v_mfma_f32_16x16x128_f8f6f4 v[52:55], v[16:23], v[226:233], v[52:55]
	v_mfma_f32_16x16x128_f8f6f4 v[44:47], v[24:31], v[234:241], v[44:47]
	v_mfma_f32_16x16x128_f8f6f4 v[36:39], v[16:23], v[234:241], v[36:39]
	v_mfma_f32_16x16x128_f8f6f4 v[88:91], v[8:15], v[210:217], v[88:91]
	v_mfma_f32_16x16x128_f8f6f4 v[80:83], v[0:7], v[210:217], v[80:83]
	v_mfma_f32_16x16x128_f8f6f4 v[72:75], v[8:15], v[218:225], v[72:75]
	v_mfma_f32_16x16x128_f8f6f4 v[64:67], v[0:7], v[218:225], v[64:67]
	v_mfma_f32_16x16x128_f8f6f4 v[56:59], v[8:15], v[226:233], v[56:59]
	v_mfma_f32_16x16x128_f8f6f4 v[48:51], v[0:7], v[226:233], v[48:51]
	v_mfma_f32_16x16x128_f8f6f4 v[40:43], v[8:15], v[234:241], v[40:43]
	v_mfma_f32_16x16x128_f8f6f4 v[32:35], v[0:7], v[234:241], v[32:35]
	s_setprio 0
	s_barrier
	s_add_i32 s38, 0, 0x18000
	s_add_i32 s39, 0, 0x1c000
	ds_read_b128 v[0:3], v252 offset:32768
	ds_read_b128 v[4:7], v253 offset:32768
	ds_read_b128 v[8:11], v252 offset:34816
	ds_read_b128 v[12:15], v253 offset:34816
	ds_read_b128 v[16:19], v252 offset:49152
	ds_read_b128 v[20:23], v253 offset:49152
	ds_read_b128 v[24:27], v252 offset:51200
	ds_read_b128 v[28:31], v253 offset:51200
	s_mov_b32 m0, s63
	v_lshl_add_u64 v[180:181], s[36:37], 0, v[180:181]
	ds_read_b128 v[210:213], v201 offset:32768
	ds_read_b128 v[218:221], v201 offset:34816
	ds_read_b128 v[214:217], v202 offset:32768
	ds_read_b128 v[222:225], v202 offset:34816
	ds_read_b128 v[226:229], v201 offset:36864
	ds_read_b128 v[234:237], v201 offset:38912
	ds_read_b128 v[230:233], v202 offset:36864
	ds_read_b128 v[238:241], v202 offset:38912
	global_load_lds_dwordx4 v[180:181], off
	v_lshl_add_u64 v[178:179], s[36:37], 0, v[178:179]
	s_mov_b32 m0, s64
	s_nop 0
	global_load_lds_dwordx4 v[178:179], off
	s_waitcnt vmcnt(8)
	s_waitcnt lgkmcnt(0)
	s_barrier
	s_setprio 1
	s_waitcnt lgkmcnt(0)
	v_mfma_f32_16x16x128_f8f6f4 v[156:159], v[0:7], v[210:217], v[156:159]
	v_mfma_f32_16x16x128_f8f6f4 v[148:151], v[8:15], v[210:217], v[148:151]
	v_mfma_f32_16x16x128_f8f6f4 v[140:143], v[0:7], v[218:225], v[140:143]
	v_mfma_f32_16x16x128_f8f6f4 v[132:135], v[8:15], v[218:225], v[132:135]
	v_mfma_f32_16x16x128_f8f6f4 v[124:127], v[0:7], v[226:233], v[124:127]
	v_mfma_f32_16x16x128_f8f6f4 v[116:119], v[8:15], v[226:233], v[116:119]
	v_mfma_f32_16x16x128_f8f6f4 v[108:111], v[0:7], v[234:241], v[108:111]
	v_mfma_f32_16x16x128_f8f6f4 v[100:103], v[8:15], v[234:241], v[100:103]
	v_mfma_f32_16x16x128_f8f6f4 v[152:155], v[16:23], v[210:217], v[152:155]
	v_mfma_f32_16x16x128_f8f6f4 v[144:147], v[24:31], v[210:217], v[144:147]
	v_mfma_f32_16x16x128_f8f6f4 v[136:139], v[16:23], v[218:225], v[136:139]
	v_mfma_f32_16x16x128_f8f6f4 v[128:131], v[24:31], v[218:225], v[128:131]
	v_mfma_f32_16x16x128_f8f6f4 v[120:123], v[16:23], v[226:233], v[120:123]
	v_mfma_f32_16x16x128_f8f6f4 v[112:115], v[24:31], v[226:233], v[112:115]
	v_mfma_f32_16x16x128_f8f6f4 v[104:107], v[16:23], v[234:241], v[104:107]
	v_mfma_f32_16x16x128_f8f6f4 v[96:99], v[24:31], v[234:241], v[96:99]
	s_setprio 0
	s_barrier
	s_add_i32 s36, s38, s44
	v_lshl_add_u64 v[178:179], v[182:183], 0, s[16:17]
	s_mov_b32 m0, s36
	ds_read_b128 v[210:213], v201 offset:49152
	ds_read_b128 v[218:221], v201 offset:51200
	ds_read_b128 v[214:217], v202 offset:49152
	ds_read_b128 v[222:225], v202 offset:51200
	ds_read_b128 v[226:229], v201 offset:53248
	ds_read_b128 v[234:237], v201 offset:55296
	ds_read_b128 v[230:233], v202 offset:53248
	ds_read_b128 v[238:241], v202 offset:55296
	global_load_lds_dwordx4 v[178:179], off
	v_lshl_add_u64 v[178:179], v[184:185], 0, s[16:17]
	s_add_i32 m0, s36, 0x2000
	s_add_i32 s36, s39, s44
	global_load_lds_dwordx4 v[178:179], off
	v_lshl_add_u64 v[178:179], v[186:187], 0, s[16:17]
	s_mov_b32 m0, s36
	s_nop 0
	global_load_lds_dwordx4 v[178:179], off
	v_lshl_add_u64 v[178:179], v[188:189], 0, s[16:17]
	s_add_i32 m0, s36, 0x2000
	s_nop 0
	global_load_lds_dwordx4 v[178:179], off
	v_lshl_add_u64 v[178:179], v[192:193], 0, s[16:17]
	s_mov_b32 m0, s65
	s_nop 0
	global_load_lds_dwordx4 v[178:179], off
	v_lshl_add_u64 v[178:179], v[190:191], 0, s[16:17]
	s_mov_b32 m0, s66
	s_nop 0
	global_load_lds_dwordx4 v[178:179], off
	s_waitcnt vmcnt(8)
	s_waitcnt lgkmcnt(0)
	s_barrier
	s_setprio 1
	s_waitcnt lgkmcnt(0)
	v_mfma_f32_16x16x128_f8f6f4 v[92:95], v[0:7], v[210:217], v[92:95]
	v_mfma_f32_16x16x128_f8f6f4 v[84:87], v[8:15], v[210:217], v[84:87]
	v_mfma_f32_16x16x128_f8f6f4 v[76:79], v[0:7], v[218:225], v[76:79]
	v_mfma_f32_16x16x128_f8f6f4 v[68:71], v[8:15], v[218:225], v[68:71]
	v_mfma_f32_16x16x128_f8f6f4 v[60:63], v[0:7], v[226:233], v[60:63]
	v_mfma_f32_16x16x128_f8f6f4 v[52:55], v[8:15], v[226:233], v[52:55]
	v_mfma_f32_16x16x128_f8f6f4 v[44:47], v[0:7], v[234:241], v[44:47]
	v_mfma_f32_16x16x128_f8f6f4 v[36:39], v[8:15], v[234:241], v[36:39]
	v_mfma_f32_16x16x128_f8f6f4 v[88:91], v[16:23], v[210:217], v[88:91]
	v_mfma_f32_16x16x128_f8f6f4 v[80:83], v[24:31], v[210:217], v[80:83]
	v_mfma_f32_16x16x128_f8f6f4 v[72:75], v[16:23], v[218:225], v[72:75]
	v_mfma_f32_16x16x128_f8f6f4 v[64:67], v[24:31], v[218:225], v[64:67]
	v_mfma_f32_16x16x128_f8f6f4 v[56:59], v[16:23], v[226:233], v[56:59]
	v_mfma_f32_16x16x128_f8f6f4 v[48:51], v[24:31], v[226:233], v[48:51]
	v_mfma_f32_16x16x128_f8f6f4 v[40:43], v[16:23], v[234:241], v[40:43]
	v_mfma_f32_16x16x128_f8f6f4 v[32:35], v[24:31], v[234:241], v[32:35]
	s_setprio 0
	s_barrier
	s_add_i32 s89, s89, 2
	s_add_u32 s4, s4, 0x100
	s_addc_u32 s5, s5, 0
	s_cmp_gt_u32 s89, 5
	s_cbranch_scc1 .LBB0_593

.LBB0_671:
	s_add_u32 s27, s34, 0x100
	s_addc_u32 s82, s35, 0
	v_mov_b32_e32 v167, v165
	v_mov_b32_e32 v169, v165
	s_add_u32 s83, s38, 0x100
	v_mov_b32_e32 v32, 0
	v_mov_b32_e32 v175, v165
	v_mov_b32_e32 v177, v165
	v_lshl_add_u64 v[178:179], s[16:17], 0, v[168:169]
	v_lshl_add_u64 v[180:181], s[16:17], 0, v[166:167]
	s_addc_u32 s84, s39, 0
	s_mov_b32 s85, -2
	s_mov_b64 s[34:35], 0
	v_mov_b32_e32 v33, v32
	v_mov_b32_e32 v34, v32
	v_mov_b32_e32 v35, v32
	v_mov_b32_e32 v36, v32
	v_mov_b32_e32 v37, v32
	v_mov_b32_e32 v38, v32
	v_mov_b32_e32 v39, v32
	v_mov_b32_e32 v48, v32
	v_mov_b32_e32 v49, v32
	v_mov_b32_e32 v50, v32
	v_mov_b32_e32 v51, v32
	v_mov_b32_e32 v52, v32
	v_mov_b32_e32 v53, v32
	v_mov_b32_e32 v54, v32
	v_mov_b32_e32 v55, v32
	v_mov_b32_e32 v64, v32
	v_mov_b32_e32 v65, v32
	v_mov_b32_e32 v66, v32
	v_mov_b32_e32 v67, v32
	v_mov_b32_e32 v68, v32
	v_mov_b32_e32 v69, v32
	v_mov_b32_e32 v70, v32
	v_mov_b32_e32 v71, v32
	v_mov_b32_e32 v80, v32
	v_mov_b32_e32 v81, v32
	v_mov_b32_e32 v82, v32
	v_mov_b32_e32 v83, v32
	v_mov_b32_e32 v84, v32
	v_mov_b32_e32 v85, v32
	v_mov_b32_e32 v86, v32
	v_mov_b32_e32 v87, v32
	v_mov_b32_e32 v40, v32
	v_mov_b32_e32 v41, v32
	v_mov_b32_e32 v42, v32
	v_mov_b32_e32 v43, v32
	v_mov_b32_e32 v44, v32
	v_mov_b32_e32 v45, v32
	v_mov_b32_e32 v46, v32
	v_mov_b32_e32 v47, v32
	v_mov_b32_e32 v56, v32
	v_mov_b32_e32 v57, v32
	v_mov_b32_e32 v58, v32
	v_mov_b32_e32 v59, v32
	v_mov_b32_e32 v60, v32
	v_mov_b32_e32 v61, v32
	v_mov_b32_e32 v62, v32
	v_mov_b32_e32 v63, v32
	v_mov_b32_e32 v72, v32
	v_mov_b32_e32 v73, v32
	v_mov_b32_e32 v74, v32
	v_mov_b32_e32 v75, v32
	v_mov_b32_e32 v76, v32
	v_mov_b32_e32 v77, v32
	v_mov_b32_e32 v78, v32
	v_mov_b32_e32 v79, v32
	v_mov_b32_e32 v88, v32
	v_mov_b32_e32 v89, v32
	v_mov_b32_e32 v90, v32
	v_mov_b32_e32 v91, v32
	v_mov_b32_e32 v92, v32
	v_mov_b32_e32 v93, v32
	v_mov_b32_e32 v94, v32
	v_mov_b32_e32 v95, v32
	v_mov_b32_e32 v96, v32
	v_mov_b32_e32 v97, v32
	v_mov_b32_e32 v98, v32
	v_mov_b32_e32 v99, v32
	v_mov_b32_e32 v100, v32
	v_mov_b32_e32 v101, v32
	v_mov_b32_e32 v102, v32
	v_mov_b32_e32 v103, v32
	v_mov_b32_e32 v112, v32
	v_mov_b32_e32 v113, v32
	v_mov_b32_e32 v114, v32
	v_mov_b32_e32 v115, v32
	v_mov_b32_e32 v116, v32
	v_mov_b32_e32 v117, v32
	v_mov_b32_e32 v118, v32
	v_mov_b32_e32 v119, v32
	v_mov_b32_e32 v128, v32
	v_mov_b32_e32 v129, v32
	v_mov_b32_e32 v130, v32
	v_mov_b32_e32 v131, v32
	v_mov_b32_e32 v132, v32
	v_mov_b32_e32 v133, v32
	v_mov_b32_e32 v134, v32
	v_mov_b32_e32 v135, v32
	v_mov_b32_e32 v144, v32
	v_mov_b32_e32 v145, v32
	v_mov_b32_e32 v146, v32
	v_mov_b32_e32 v147, v32
	v_mov_b32_e32 v148, v32
	v_mov_b32_e32 v149, v32
	v_mov_b32_e32 v150, v32
	v_mov_b32_e32 v151, v32
	v_mov_b32_e32 v104, v32
	v_mov_b32_e32 v105, v32
	v_mov_b32_e32 v106, v32
	v_mov_b32_e32 v107, v32
	v_mov_b32_e32 v108, v32
	v_mov_b32_e32 v109, v32
	v_mov_b32_e32 v110, v32
	v_mov_b32_e32 v111, v32
	v_mov_b32_e32 v120, v32
	v_mov_b32_e32 v121, v32
	v_mov_b32_e32 v122, v32
	v_mov_b32_e32 v123, v32
	v_mov_b32_e32 v124, v32
	v_mov_b32_e32 v125, v32
	v_mov_b32_e32 v126, v32
	v_mov_b32_e32 v127, v32
	v_mov_b32_e32 v136, v32
	v_mov_b32_e32 v137, v32
	v_mov_b32_e32 v138, v32
	v_mov_b32_e32 v139, v32
	v_mov_b32_e32 v140, v32
	v_mov_b32_e32 v141, v32
	v_mov_b32_e32 v142, v32
	v_mov_b32_e32 v143, v32
	v_mov_b32_e32 v152, v32
	v_mov_b32_e32 v153, v32
	v_mov_b32_e32 v154, v32
	v_mov_b32_e32 v155, v32
	v_mov_b32_e32 v156, v32
	v_mov_b32_e32 v157, v32
	v_mov_b32_e32 v158, v32
	v_mov_b32_e32 v159, v32
	v_add_u32_e32 v252, 0x10000, v205
	v_add_u32_e32 v253, 0x10000, v206
	s_branch .LBB0_673
.LBB0_672:
	s_add_u32 s36, s6, s34
	s_addc_u32 s37, s7, s35
	s_add_u32 s38, s36, 0x12c00100
	s_addc_u32 s39, s37, 0
	ds_read_b128 v[24:27], v252
	ds_read_b128 v[28:31], v253
	s_and_b64 s[36:37], s[40:41], exec
	ds_read_b128 v[16:19], v252 offset:2048
	ds_read_b128 v[20:23], v253 offset:2048
	s_cselect_b32 s37, s9, s39
	s_cselect_b32 s36, s8, s38
	s_add_u32 s86, s27, s34
	ds_read_b128 v[8:11], v252 offset:16384
	ds_read_b128 v[12:15], v253 offset:16384
	s_addc_u32 s87, s82, s35
	ds_read_b128 v[0:3], v252 offset:18432
	ds_read_b128 v[4:7], v253 offset:18432
	s_and_b64 s[38:39], s[40:41], exec
	s_cselect_b32 s39, s29, s87
	s_cselect_b32 s38, s28, s86
	s_add_u32 s86, s83, s34
	s_addc_u32 s87, s84, s35
	s_and_b64 s[40:41], s[40:41], exec
	s_cselect_b32 s41, s31, s87
	s_cselect_b32 s40, s30, s86
	v_lshl_add_u64 v[194:195], v[180:181], 0, s[34:35]
	s_add_i32 m0, s59, 0xc000
	ds_read_b128 v[186:189], v207
	ds_read_b128 v[216:219], v207 offset:2048
	ds_read_b128 v[190:193], v208
	ds_read_b128 v[220:223], v208 offset:2048
	ds_read_b128 v[224:227], v207 offset:4096
	ds_read_b128 v[232:235], v207 offset:6144
	ds_read_b128 v[228:231], v208 offset:4096
	ds_read_b128 v[236:239], v208 offset:6144
	global_load_lds_dwordx4 v[194:195], off
	v_lshl_add_u64 v[194:195], v[178:179], 0, s[34:35]
	s_add_i32 m0, s59, 0xe000
	s_nop 0
	global_load_lds_dwordx4 v[194:195], off
	s_waitcnt vmcnt(8)
	s_waitcnt lgkmcnt(0)
	s_barrier
	s_setprio 1
	s_waitcnt lgkmcnt(0)
	v_mfma_f32_16x16x128_f8f6f4 v[156:159], v[24:31], v[186:193], v[156:159]
	v_mfma_f32_16x16x128_f8f6f4 v[152:155], v[16:23], v[186:193], v[152:155]
	v_mfma_f32_16x16x128_f8f6f4 v[140:143], v[24:31], v[216:223], v[140:143]
	v_mfma_f32_16x16x128_f8f6f4 v[136:139], v[16:23], v[216:223], v[136:139]
	v_mfma_f32_16x16x128_f8f6f4 v[124:127], v[24:31], v[224:231], v[124:127]
	v_mfma_f32_16x16x128_f8f6f4 v[120:123], v[16:23], v[224:231], v[120:123]
	v_mfma_f32_16x16x128_f8f6f4 v[108:111], v[24:31], v[232:239], v[108:111]
	v_mfma_f32_16x16x128_f8f6f4 v[104:107], v[16:23], v[232:239], v[104:107]
	v_mfma_f32_16x16x128_f8f6f4 v[148:151], v[8:15], v[186:193], v[148:151]
	v_mfma_f32_16x16x128_f8f6f4 v[144:147], v[0:7], v[186:193], v[144:147]
	v_mfma_f32_16x16x128_f8f6f4 v[132:135], v[8:15], v[216:223], v[132:135]
	v_mfma_f32_16x16x128_f8f6f4 v[128:131], v[0:7], v[216:223], v[128:131]
	v_mfma_f32_16x16x128_f8f6f4 v[116:119], v[8:15], v[224:231], v[116:119]
	v_mfma_f32_16x16x128_f8f6f4 v[112:115], v[0:7], v[224:231], v[112:115]
	v_mfma_f32_16x16x128_f8f6f4 v[100:103], v[8:15], v[232:239], v[100:103]
	v_mfma_f32_16x16x128_f8f6f4 v[96:99], v[0:7], v[232:239], v[96:99]
	s_setprio 0
	s_barrier
	s_add_i32 s86, s69, s42
	v_lshl_add_u64 v[186:187], s[38:39], 0, v[160:161]
	s_mov_b32 m0, s86
	ds_read_b128 v[216:219], v207 offset:16384
	ds_read_b128 v[224:227], v207 offset:18432
	ds_read_b128 v[220:223], v208 offset:16384
	ds_read_b128 v[228:231], v208 offset:18432
	ds_read_b128 v[232:235], v207 offset:20480
	ds_read_b128 v[240:243], v207 offset:22528
	ds_read_b128 v[236:239], v208 offset:20480
	ds_read_b128 v[244:247], v208 offset:22528
	global_load_lds_dwordx4 v[186:187], off
	v_lshl_add_u64 v[188:189], s[38:39], 0, v[162:163]
	s_add_i32 m0, s86, 0x2000
	s_add_i32 s38, s71, s42
	global_load_lds_dwordx4 v[188:189], off
	v_lshl_add_u64 v[190:191], s[40:41], 0, v[160:161]
	s_mov_b32 m0, s38
	v_lshl_add_u64 v[192:193], s[40:41], 0, v[162:163]
	global_load_lds_dwordx4 v[190:191], off
	s_add_i32 m0, s38, 0x2000
	v_mov_b32_e32 v173, v165
	global_load_lds_dwordx4 v[192:193], off
	s_mov_b32 m0, s59
	v_lshl_add_u64 v[196:197], s[36:37], 0, v[164:165]
	global_load_lds_dwordx4 v164, s[36:37]
	s_mov_b32 m0, s60
	v_lshl_add_u64 v[194:195], s[36:37], 0, v[172:173]
	global_load_lds_dwordx4 v172, s[36:37]
	s_waitcnt vmcnt(8)
	s_waitcnt lgkmcnt(0)
	s_barrier
	s_setprio 1
	s_waitcnt lgkmcnt(0)
	v_mfma_f32_16x16x128_f8f6f4 v[92:95], v[24:31], v[216:223], v[92:95]
	v_mfma_f32_16x16x128_f8f6f4 v[88:91], v[16:23], v[216:223], v[88:91]
	v_mfma_f32_16x16x128_f8f6f4 v[76:79], v[24:31], v[224:231], v[76:79]
	v_mfma_f32_16x16x128_f8f6f4 v[72:75], v[16:23], v[224:231], v[72:75]
	v_mfma_f32_16x16x128_f8f6f4 v[60:63], v[24:31], v[232:239], v[60:63]
	v_mfma_f32_16x16x128_f8f6f4 v[56:59], v[16:23], v[232:239], v[56:59]
	v_mfma_f32_16x16x128_f8f6f4 v[44:47], v[24:31], v[240:247], v[44:47]
	v_mfma_f32_16x16x128_f8f6f4 v[40:43], v[16:23], v[240:247], v[40:43]
	v_mfma_f32_16x16x128_f8f6f4 v[84:87], v[8:15], v[216:223], v[84:87]
	v_mfma_f32_16x16x128_f8f6f4 v[80:83], v[0:7], v[216:223], v[80:83]
	v_mfma_f32_16x16x128_f8f6f4 v[68:71], v[8:15], v[224:231], v[68:71]
	v_mfma_f32_16x16x128_f8f6f4 v[64:67], v[0:7], v[224:231], v[64:67]
	v_mfma_f32_16x16x128_f8f6f4 v[52:55], v[8:15], v[232:239], v[52:55]
	v_mfma_f32_16x16x128_f8f6f4 v[48:51], v[0:7], v[232:239], v[48:51]
	v_mfma_f32_16x16x128_f8f6f4 v[36:39], v[8:15], v[240:247], v[36:39]
	v_mfma_f32_16x16x128_f8f6f4 v[32:35], v[0:7], v[240:247], v[32:35]
	s_setprio 0
	s_barrier
	s_add_i32 s38, 0, 0x18000
	s_add_i32 s39, 0, 0x1c000
	ds_read_b128 v[0:3], v252 offset:32768
	ds_read_b128 v[4:7], v253 offset:32768
	ds_read_b128 v[8:11], v252 offset:34816
	ds_read_b128 v[12:15], v253 offset:34816
	ds_read_b128 v[16:19], v252 offset:49152
	ds_read_b128 v[20:23], v253 offset:49152
	ds_read_b128 v[24:27], v252 offset:51200
	ds_read_b128 v[28:31], v253 offset:51200
	s_mov_b32 m0, s61
	v_lshl_add_u64 v[184:185], s[36:37], 0, v[184:185]
	ds_read_b128 v[216:219], v207 offset:32768
	ds_read_b128 v[224:227], v207 offset:34816
	ds_read_b128 v[220:223], v208 offset:32768
	ds_read_b128 v[228:231], v208 offset:34816
	ds_read_b128 v[232:235], v207 offset:36864
	ds_read_b128 v[240:243], v207 offset:38912
	ds_read_b128 v[236:239], v208 offset:36864
	ds_read_b128 v[244:247], v208 offset:38912
	global_load_lds_dwordx4 v[184:185], off
	v_lshl_add_u64 v[182:183], s[36:37], 0, v[182:183]
	s_mov_b32 m0, s62
	s_nop 0
	global_load_lds_dwordx4 v[182:183], off
	s_waitcnt vmcnt(8)
	s_waitcnt lgkmcnt(0)
	s_barrier
	s_setprio 1
	s_waitcnt lgkmcnt(0)
	v_mfma_f32_16x16x128_f8f6f4 v[156:159], v[0:7], v[216:223], v[156:159]
	v_mfma_f32_16x16x128_f8f6f4 v[152:155], v[8:15], v[216:223], v[152:155]
	v_mfma_f32_16x16x128_f8f6f4 v[140:143], v[0:7], v[224:231], v[140:143]
	v_mfma_f32_16x16x128_f8f6f4 v[136:139], v[8:15], v[224:231], v[136:139]
	v_mfma_f32_16x16x128_f8f6f4 v[124:127], v[0:7], v[232:239], v[124:127]
	v_mfma_f32_16x16x128_f8f6f4 v[120:123], v[8:15], v[232:239], v[120:123]
	v_mfma_f32_16x16x128_f8f6f4 v[108:111], v[0:7], v[240:247], v[108:111]
	v_mfma_f32_16x16x128_f8f6f4 v[104:107], v[8:15], v[240:247], v[104:107]
	v_mfma_f32_16x16x128_f8f6f4 v[148:151], v[16:23], v[216:223], v[148:151]
	v_mfma_f32_16x16x128_f8f6f4 v[144:147], v[24:31], v[216:223], v[144:147]
	v_mfma_f32_16x16x128_f8f6f4 v[132:135], v[16:23], v[224:231], v[132:135]
	v_mfma_f32_16x16x128_f8f6f4 v[128:131], v[24:31], v[224:231], v[128:131]
	v_mfma_f32_16x16x128_f8f6f4 v[116:119], v[16:23], v[232:239], v[116:119]
	v_mfma_f32_16x16x128_f8f6f4 v[112:115], v[24:31], v[232:239], v[112:115]
	v_mfma_f32_16x16x128_f8f6f4 v[100:103], v[16:23], v[240:247], v[100:103]
	v_mfma_f32_16x16x128_f8f6f4 v[96:99], v[24:31], v[240:247], v[96:99]
	s_setprio 0
	s_barrier
	s_add_i32 s36, s38, s42
	v_lshl_add_u64 v[182:183], v[186:187], 0, s[14:15]
	s_mov_b32 m0, s36
	ds_read_b128 v[216:219], v207 offset:49152
	ds_read_b128 v[224:227], v207 offset:51200
	ds_read_b128 v[220:223], v208 offset:49152
	ds_read_b128 v[228:231], v208 offset:51200
	ds_read_b128 v[232:235], v207 offset:53248
	ds_read_b128 v[240:243], v207 offset:55296
	ds_read_b128 v[236:239], v208 offset:53248
	ds_read_b128 v[244:247], v208 offset:55296
	global_load_lds_dwordx4 v[182:183], off
	v_lshl_add_u64 v[182:183], v[188:189], 0, s[14:15]
	s_add_i32 m0, s36, 0x2000
	s_add_i32 s36, s39, s42
	global_load_lds_dwordx4 v[182:183], off
	v_lshl_add_u64 v[182:183], v[190:191], 0, s[14:15]
	s_mov_b32 m0, s36
	s_nop 0
	global_load_lds_dwordx4 v[182:183], off
	v_lshl_add_u64 v[182:183], v[192:193], 0, s[14:15]
	s_add_i32 m0, s36, 0x2000
	s_nop 0
	global_load_lds_dwordx4 v[182:183], off
	v_lshl_add_u64 v[182:183], v[196:197], 0, s[14:15]
	s_mov_b32 m0, s63
	s_nop 0
	global_load_lds_dwordx4 v[182:183], off
	v_lshl_add_u64 v[182:183], v[194:195], 0, s[14:15]
	s_mov_b32 m0, s64
	s_nop 0
	global_load_lds_dwordx4 v[182:183], off
	s_waitcnt vmcnt(8)
	s_waitcnt lgkmcnt(0)
	s_barrier
	s_setprio 1
	s_waitcnt lgkmcnt(0)
	v_mfma_f32_16x16x128_f8f6f4 v[92:95], v[0:7], v[216:223], v[92:95]
	v_mfma_f32_16x16x128_f8f6f4 v[88:91], v[8:15], v[216:223], v[88:91]
	v_mfma_f32_16x16x128_f8f6f4 v[76:79], v[0:7], v[224:231], v[76:79]
	v_mfma_f32_16x16x128_f8f6f4 v[72:75], v[8:15], v[224:231], v[72:75]
	v_mfma_f32_16x16x128_f8f6f4 v[60:63], v[0:7], v[232:239], v[60:63]
	v_mfma_f32_16x16x128_f8f6f4 v[56:59], v[8:15], v[232:239], v[56:59]
	v_mfma_f32_16x16x128_f8f6f4 v[44:47], v[0:7], v[240:247], v[44:47]
	v_mfma_f32_16x16x128_f8f6f4 v[40:43], v[8:15], v[240:247], v[40:43]
	v_mfma_f32_16x16x128_f8f6f4 v[84:87], v[16:23], v[216:223], v[84:87]
	v_mfma_f32_16x16x128_f8f6f4 v[80:83], v[24:31], v[216:223], v[80:83]
	v_mfma_f32_16x16x128_f8f6f4 v[68:71], v[16:23], v[224:231], v[68:71]
	v_mfma_f32_16x16x128_f8f6f4 v[64:67], v[24:31], v[224:231], v[64:67]
	v_mfma_f32_16x16x128_f8f6f4 v[52:55], v[16:23], v[232:239], v[52:55]
	v_mfma_f32_16x16x128_f8f6f4 v[48:51], v[24:31], v[232:239], v[48:51]
	v_mfma_f32_16x16x128_f8f6f4 v[36:39], v[16:23], v[240:247], v[36:39]
	v_mfma_f32_16x16x128_f8f6f4 v[32:35], v[24:31], v[240:247], v[32:35]
	s_setprio 0
	s_barrier
	s_add_i32 s85, s85, 2
	s_add_u32 s34, s34, 0x100
	s_addc_u32 s35, s35, 0
	s_cmp_gt_u32 s85, 5
	s_cbranch_scc1 .LBB0_675

.LBB0_816:
	s_add_u32 s56, s26, 0x100
	s_addc_u32 s57, s27, 0
	v_mov_b32_e32 v169, v165
	v_mov_b32_e32 v171, v165
	s_add_u32 s58, s28, 0x100
	v_mov_b32_e32 v32, 0
	v_mov_b32_e32 v175, v165
	v_mov_b32_e32 v177, v165
	v_lshl_add_u64 v[178:179], s[14:15], 0, v[170:171]
	v_lshl_add_u64 v[180:181], s[14:15], 0, v[168:169]
	s_addc_u32 s59, s29, 0
	s_mov_b32 s60, -2
	s_mov_b64 s[26:27], 0
	v_mov_b32_e32 v33, v32
	v_mov_b32_e32 v34, v32
	v_mov_b32_e32 v35, v32
	v_mov_b32_e32 v36, v32
	v_mov_b32_e32 v37, v32
	v_mov_b32_e32 v38, v32
	v_mov_b32_e32 v39, v32
	v_mov_b32_e32 v48, v32
	v_mov_b32_e32 v49, v32
	v_mov_b32_e32 v50, v32
	v_mov_b32_e32 v51, v32
	v_mov_b32_e32 v52, v32
	v_mov_b32_e32 v53, v32
	v_mov_b32_e32 v54, v32
	v_mov_b32_e32 v55, v32
	v_mov_b32_e32 v64, v32
	v_mov_b32_e32 v65, v32
	v_mov_b32_e32 v66, v32
	v_mov_b32_e32 v67, v32
	v_mov_b32_e32 v68, v32
	v_mov_b32_e32 v69, v32
	v_mov_b32_e32 v70, v32
	v_mov_b32_e32 v71, v32
	v_mov_b32_e32 v80, v32
	v_mov_b32_e32 v81, v32
	v_mov_b32_e32 v82, v32
	v_mov_b32_e32 v83, v32
	v_mov_b32_e32 v84, v32
	v_mov_b32_e32 v85, v32
	v_mov_b32_e32 v86, v32
	v_mov_b32_e32 v87, v32
	v_mov_b32_e32 v40, v32
	v_mov_b32_e32 v41, v32
	v_mov_b32_e32 v42, v32
	v_mov_b32_e32 v43, v32
	v_mov_b32_e32 v44, v32
	v_mov_b32_e32 v45, v32
	v_mov_b32_e32 v46, v32
	v_mov_b32_e32 v47, v32
	v_mov_b32_e32 v56, v32
	v_mov_b32_e32 v57, v32
	v_mov_b32_e32 v58, v32
	v_mov_b32_e32 v59, v32
	v_mov_b32_e32 v60, v32
	v_mov_b32_e32 v61, v32
	v_mov_b32_e32 v62, v32
	v_mov_b32_e32 v63, v32
	v_mov_b32_e32 v72, v32
	v_mov_b32_e32 v73, v32
	v_mov_b32_e32 v74, v32
	v_mov_b32_e32 v75, v32
	v_mov_b32_e32 v76, v32
	v_mov_b32_e32 v77, v32
	v_mov_b32_e32 v78, v32
	v_mov_b32_e32 v79, v32
	v_mov_b32_e32 v88, v32
	v_mov_b32_e32 v89, v32
	v_mov_b32_e32 v90, v32
	v_mov_b32_e32 v91, v32
	v_mov_b32_e32 v92, v32
	v_mov_b32_e32 v93, v32
	v_mov_b32_e32 v94, v32
	v_mov_b32_e32 v95, v32
	v_mov_b32_e32 v96, v32
	v_mov_b32_e32 v97, v32
	v_mov_b32_e32 v98, v32
	v_mov_b32_e32 v99, v32
	v_mov_b32_e32 v100, v32
	v_mov_b32_e32 v101, v32
	v_mov_b32_e32 v102, v32
	v_mov_b32_e32 v103, v32
	v_mov_b32_e32 v112, v32
	v_mov_b32_e32 v113, v32
	v_mov_b32_e32 v114, v32
	v_mov_b32_e32 v115, v32
	v_mov_b32_e32 v116, v32
	v_mov_b32_e32 v117, v32
	v_mov_b32_e32 v118, v32
	v_mov_b32_e32 v119, v32
	v_mov_b32_e32 v128, v32
	v_mov_b32_e32 v129, v32
	v_mov_b32_e32 v130, v32
	v_mov_b32_e32 v131, v32
	v_mov_b32_e32 v132, v32
	v_mov_b32_e32 v133, v32
	v_mov_b32_e32 v134, v32
	v_mov_b32_e32 v135, v32
	v_mov_b32_e32 v144, v32
	v_mov_b32_e32 v145, v32
	v_mov_b32_e32 v146, v32
	v_mov_b32_e32 v147, v32
	v_mov_b32_e32 v148, v32
	v_mov_b32_e32 v149, v32
	v_mov_b32_e32 v150, v32
	v_mov_b32_e32 v151, v32
	v_mov_b32_e32 v104, v32
	v_mov_b32_e32 v105, v32
	v_mov_b32_e32 v106, v32
	v_mov_b32_e32 v107, v32
	v_mov_b32_e32 v108, v32
	v_mov_b32_e32 v109, v32
	v_mov_b32_e32 v110, v32
	v_mov_b32_e32 v111, v32
	v_mov_b32_e32 v120, v32
	v_mov_b32_e32 v121, v32
	v_mov_b32_e32 v122, v32
	v_mov_b32_e32 v123, v32
	v_mov_b32_e32 v124, v32
	v_mov_b32_e32 v125, v32
	v_mov_b32_e32 v126, v32
	v_mov_b32_e32 v127, v32
	v_mov_b32_e32 v136, v32
	v_mov_b32_e32 v137, v32
	v_mov_b32_e32 v138, v32
	v_mov_b32_e32 v139, v32
	v_mov_b32_e32 v140, v32
	v_mov_b32_e32 v141, v32
	v_mov_b32_e32 v142, v32
	v_mov_b32_e32 v143, v32
	v_mov_b32_e32 v152, v32
	v_mov_b32_e32 v153, v32
	v_mov_b32_e32 v154, v32
	v_mov_b32_e32 v155, v32
	v_mov_b32_e32 v156, v32
	v_mov_b32_e32 v157, v32
	v_mov_b32_e32 v158, v32
	v_mov_b32_e32 v159, v32
	v_add_u32_e32 v252, 0x10000, v173
	v_add_u32_e32 v253, 0x10000, v206
	s_branch .LBB0_818
.LBB0_817:
	s_add_u32 s28, s10, s26
	s_addc_u32 s29, s11, s27
	s_add_u32 s30, s28, 0x38000100
	s_addc_u32 s31, s29, 0
	ds_read_b128 v[24:27], v252
	ds_read_b128 v[28:31], v253
	s_and_b64 s[28:29], s[34:35], exec
	ds_read_b128 v[16:19], v252 offset:2048
	ds_read_b128 v[20:23], v253 offset:2048
	s_cselect_b32 s29, s1, s31
	s_cselect_b32 s28, s0, s30
	s_add_u32 s61, s56, s26
	ds_read_b128 v[8:11], v252 offset:16384
	ds_read_b128 v[12:15], v253 offset:16384
	s_addc_u32 s62, s57, s27
	ds_read_b128 v[0:3], v252 offset:18432
	ds_read_b128 v[4:7], v253 offset:18432
	s_and_b64 s[30:31], s[34:35], exec
	s_cselect_b32 s31, s23, s62
	s_cselect_b32 s30, s22, s61
	s_add_u32 s61, s58, s26
	s_addc_u32 s62, s59, s27
	s_and_b64 s[34:35], s[34:35], exec
	s_cselect_b32 s35, s25, s62
	s_cselect_b32 s34, s24, s61
	v_lshl_add_u64 v[194:195], v[180:181], 0, s[26:27]
	s_add_i32 m0, s37, 0xc000
	ds_read_b128 v[186:189], v207
	ds_read_b128 v[216:219], v207 offset:2048
	ds_read_b128 v[190:193], v208
	ds_read_b128 v[220:223], v208 offset:2048
	ds_read_b128 v[224:227], v207 offset:4096
	ds_read_b128 v[232:235], v207 offset:6144
	ds_read_b128 v[228:231], v208 offset:4096
	ds_read_b128 v[236:239], v208 offset:6144
	global_load_lds_dwordx4 v[194:195], off
	v_lshl_add_u64 v[194:195], v[178:179], 0, s[26:27]
	s_add_i32 m0, s37, 0xe000
	s_nop 0
	global_load_lds_dwordx4 v[194:195], off
	s_waitcnt vmcnt(8)
	s_waitcnt lgkmcnt(0)
	s_barrier
	s_setprio 1
	s_waitcnt lgkmcnt(0)
	v_mfma_f32_16x16x128_f8f6f4 v[156:159], v[24:31], v[186:193], v[156:159]
	v_mfma_f32_16x16x128_f8f6f4 v[152:155], v[16:23], v[186:193], v[152:155]
	v_mfma_f32_16x16x128_f8f6f4 v[140:143], v[24:31], v[216:223], v[140:143]
	v_mfma_f32_16x16x128_f8f6f4 v[136:139], v[16:23], v[216:223], v[136:139]
	v_mfma_f32_16x16x128_f8f6f4 v[124:127], v[24:31], v[224:231], v[124:127]
	v_mfma_f32_16x16x128_f8f6f4 v[120:123], v[16:23], v[224:231], v[120:123]
	v_mfma_f32_16x16x128_f8f6f4 v[108:111], v[24:31], v[232:239], v[108:111]
	v_mfma_f32_16x16x128_f8f6f4 v[104:107], v[16:23], v[232:239], v[104:107]
	v_mfma_f32_16x16x128_f8f6f4 v[148:151], v[8:15], v[186:193], v[148:151]
	v_mfma_f32_16x16x128_f8f6f4 v[144:147], v[0:7], v[186:193], v[144:147]
	v_mfma_f32_16x16x128_f8f6f4 v[132:135], v[8:15], v[216:223], v[132:135]
	v_mfma_f32_16x16x128_f8f6f4 v[128:131], v[0:7], v[216:223], v[128:131]
	v_mfma_f32_16x16x128_f8f6f4 v[116:119], v[8:15], v[224:231], v[116:119]
	v_mfma_f32_16x16x128_f8f6f4 v[112:115], v[0:7], v[224:231], v[112:115]
	v_mfma_f32_16x16x128_f8f6f4 v[100:103], v[8:15], v[232:239], v[100:103]
	v_mfma_f32_16x16x128_f8f6f4 v[96:99], v[0:7], v[232:239], v[96:99]
	s_setprio 0
	s_barrier
	s_add_i32 s61, s44, s36
	v_lshl_add_u64 v[186:187], s[30:31], 0, v[160:161]
	s_mov_b32 m0, s61
	ds_read_b128 v[216:219], v207 offset:16384
	ds_read_b128 v[224:227], v207 offset:18432
	ds_read_b128 v[220:223], v208 offset:16384
	ds_read_b128 v[228:231], v208 offset:18432
	ds_read_b128 v[232:235], v207 offset:20480
	ds_read_b128 v[240:243], v207 offset:22528
	ds_read_b128 v[236:239], v208 offset:20480
	ds_read_b128 v[244:247], v208 offset:22528
	global_load_lds_dwordx4 v[186:187], off
	v_lshl_add_u64 v[188:189], s[30:31], 0, v[162:163]
	s_add_i32 m0, s61, 0x2000
	s_add_i32 s30, s46, s36
	global_load_lds_dwordx4 v[188:189], off
	v_lshl_add_u64 v[190:191], s[34:35], 0, v[160:161]
	s_mov_b32 m0, s30
	v_lshl_add_u64 v[192:193], s[34:35], 0, v[162:163]
	global_load_lds_dwordx4 v[190:191], off
	s_add_i32 m0, s30, 0x2000
	v_mov_b32_e32 v167, v165
	global_load_lds_dwordx4 v[192:193], off
	s_mov_b32 m0, s37
	v_lshl_add_u64 v[196:197], s[28:29], 0, v[164:165]
	global_load_lds_dwordx4 v164, s[28:29]
	s_mov_b32 m0, s38
	v_lshl_add_u64 v[194:195], s[28:29], 0, v[166:167]
	global_load_lds_dwordx4 v166, s[28:29]
	s_waitcnt vmcnt(8)
	s_waitcnt lgkmcnt(0)
	s_barrier
	s_setprio 1
	s_waitcnt lgkmcnt(0)
	v_mfma_f32_16x16x128_f8f6f4 v[92:95], v[24:31], v[216:223], v[92:95]
	v_mfma_f32_16x16x128_f8f6f4 v[88:91], v[16:23], v[216:223], v[88:91]
	v_mfma_f32_16x16x128_f8f6f4 v[76:79], v[24:31], v[224:231], v[76:79]
	v_mfma_f32_16x16x128_f8f6f4 v[72:75], v[16:23], v[224:231], v[72:75]
	v_mfma_f32_16x16x128_f8f6f4 v[60:63], v[24:31], v[232:239], v[60:63]
	v_mfma_f32_16x16x128_f8f6f4 v[56:59], v[16:23], v[232:239], v[56:59]
	v_mfma_f32_16x16x128_f8f6f4 v[44:47], v[24:31], v[240:247], v[44:47]
	v_mfma_f32_16x16x128_f8f6f4 v[40:43], v[16:23], v[240:247], v[40:43]
	v_mfma_f32_16x16x128_f8f6f4 v[84:87], v[8:15], v[216:223], v[84:87]
	v_mfma_f32_16x16x128_f8f6f4 v[80:83], v[0:7], v[216:223], v[80:83]
	v_mfma_f32_16x16x128_f8f6f4 v[68:71], v[8:15], v[224:231], v[68:71]
	v_mfma_f32_16x16x128_f8f6f4 v[64:67], v[0:7], v[224:231], v[64:67]
	v_mfma_f32_16x16x128_f8f6f4 v[52:55], v[8:15], v[232:239], v[52:55]
	v_mfma_f32_16x16x128_f8f6f4 v[48:51], v[0:7], v[232:239], v[48:51]
	v_mfma_f32_16x16x128_f8f6f4 v[36:39], v[8:15], v[240:247], v[36:39]
	v_mfma_f32_16x16x128_f8f6f4 v[32:35], v[0:7], v[240:247], v[32:35]
	s_setprio 0
	s_barrier
	s_add_i32 s30, 0, 0x18000
	s_add_i32 s31, 0, 0x1c000
	ds_read_b128 v[0:3], v252 offset:32768
	ds_read_b128 v[4:7], v253 offset:32768
	ds_read_b128 v[8:11], v252 offset:34816
	ds_read_b128 v[12:15], v253 offset:34816
	ds_read_b128 v[16:19], v252 offset:49152
	ds_read_b128 v[20:23], v253 offset:49152
	ds_read_b128 v[24:27], v252 offset:51200
	ds_read_b128 v[28:31], v253 offset:51200
	s_mov_b32 m0, s39
	v_lshl_add_u64 v[184:185], s[28:29], 0, v[184:185]
	ds_read_b128 v[216:219], v207 offset:32768
	ds_read_b128 v[224:227], v207 offset:34816
	ds_read_b128 v[220:223], v208 offset:32768
	ds_read_b128 v[228:231], v208 offset:34816
	ds_read_b128 v[232:235], v207 offset:36864
	ds_read_b128 v[240:243], v207 offset:38912
	ds_read_b128 v[236:239], v208 offset:36864
	ds_read_b128 v[244:247], v208 offset:38912
	global_load_lds_dwordx4 v[184:185], off
	v_lshl_add_u64 v[182:183], s[28:29], 0, v[182:183]
	s_mov_b32 m0, s40
	s_nop 0
	global_load_lds_dwordx4 v[182:183], off
	s_waitcnt vmcnt(8)
	s_waitcnt lgkmcnt(0)
	s_barrier
	s_setprio 1
	s_waitcnt lgkmcnt(0)
	v_mfma_f32_16x16x128_f8f6f4 v[156:159], v[0:7], v[216:223], v[156:159]
	v_mfma_f32_16x16x128_f8f6f4 v[152:155], v[8:15], v[216:223], v[152:155]
	v_mfma_f32_16x16x128_f8f6f4 v[140:143], v[0:7], v[224:231], v[140:143]
	v_mfma_f32_16x16x128_f8f6f4 v[136:139], v[8:15], v[224:231], v[136:139]
	v_mfma_f32_16x16x128_f8f6f4 v[124:127], v[0:7], v[232:239], v[124:127]
	v_mfma_f32_16x16x128_f8f6f4 v[120:123], v[8:15], v[232:239], v[120:123]
	v_mfma_f32_16x16x128_f8f6f4 v[108:111], v[0:7], v[240:247], v[108:111]
	v_mfma_f32_16x16x128_f8f6f4 v[104:107], v[8:15], v[240:247], v[104:107]
	v_mfma_f32_16x16x128_f8f6f4 v[148:151], v[16:23], v[216:223], v[148:151]
	v_mfma_f32_16x16x128_f8f6f4 v[144:147], v[24:31], v[216:223], v[144:147]
	v_mfma_f32_16x16x128_f8f6f4 v[132:135], v[16:23], v[224:231], v[132:135]
	v_mfma_f32_16x16x128_f8f6f4 v[128:131], v[24:31], v[224:231], v[128:131]
	v_mfma_f32_16x16x128_f8f6f4 v[116:119], v[16:23], v[232:239], v[116:119]
	v_mfma_f32_16x16x128_f8f6f4 v[112:115], v[24:31], v[232:239], v[112:115]
	v_mfma_f32_16x16x128_f8f6f4 v[100:103], v[16:23], v[240:247], v[100:103]
	v_mfma_f32_16x16x128_f8f6f4 v[96:99], v[24:31], v[240:247], v[96:99]
	s_setprio 0
	s_barrier
	s_add_i32 s28, s30, s36
	v_lshl_add_u64 v[182:183], v[186:187], 0, s[12:13]
	s_mov_b32 m0, s28
	ds_read_b128 v[216:219], v207 offset:49152
	ds_read_b128 v[224:227], v207 offset:51200
	ds_read_b128 v[220:223], v208 offset:49152
	ds_read_b128 v[228:231], v208 offset:51200
	ds_read_b128 v[232:235], v207 offset:53248
	ds_read_b128 v[240:243], v207 offset:55296
	ds_read_b128 v[236:239], v208 offset:53248
	ds_read_b128 v[244:247], v208 offset:55296
	global_load_lds_dwordx4 v[182:183], off
	v_lshl_add_u64 v[182:183], v[188:189], 0, s[12:13]
	s_add_i32 m0, s28, 0x2000
	s_add_i32 s28, s31, s36
	global_load_lds_dwordx4 v[182:183], off
	v_lshl_add_u64 v[182:183], v[190:191], 0, s[12:13]
	s_mov_b32 m0, s28
	s_nop 0
	global_load_lds_dwordx4 v[182:183], off
	v_lshl_add_u64 v[182:183], v[192:193], 0, s[12:13]
	s_add_i32 m0, s28, 0x2000
	s_nop 0
	global_load_lds_dwordx4 v[182:183], off
	v_lshl_add_u64 v[182:183], v[196:197], 0, s[12:13]
	s_mov_b32 m0, s41
	s_nop 0
	global_load_lds_dwordx4 v[182:183], off
	v_lshl_add_u64 v[182:183], v[194:195], 0, s[12:13]
	s_mov_b32 m0, s42
	s_nop 0
	global_load_lds_dwordx4 v[182:183], off
	s_waitcnt vmcnt(8)
	s_waitcnt lgkmcnt(0)
	s_barrier
	s_setprio 1
	s_waitcnt lgkmcnt(0)
	v_mfma_f32_16x16x128_f8f6f4 v[92:95], v[0:7], v[216:223], v[92:95]
	v_mfma_f32_16x16x128_f8f6f4 v[88:91], v[8:15], v[216:223], v[88:91]
	v_mfma_f32_16x16x128_f8f6f4 v[76:79], v[0:7], v[224:231], v[76:79]
	v_mfma_f32_16x16x128_f8f6f4 v[72:75], v[8:15], v[224:231], v[72:75]
	v_mfma_f32_16x16x128_f8f6f4 v[60:63], v[0:7], v[232:239], v[60:63]
	v_mfma_f32_16x16x128_f8f6f4 v[56:59], v[8:15], v[232:239], v[56:59]
	v_mfma_f32_16x16x128_f8f6f4 v[44:47], v[0:7], v[240:247], v[44:47]
	v_mfma_f32_16x16x128_f8f6f4 v[40:43], v[8:15], v[240:247], v[40:43]
	v_mfma_f32_16x16x128_f8f6f4 v[84:87], v[16:23], v[216:223], v[84:87]
	v_mfma_f32_16x16x128_f8f6f4 v[80:83], v[24:31], v[216:223], v[80:83]
	v_mfma_f32_16x16x128_f8f6f4 v[68:71], v[16:23], v[224:231], v[68:71]
	v_mfma_f32_16x16x128_f8f6f4 v[64:67], v[24:31], v[224:231], v[64:67]
	v_mfma_f32_16x16x128_f8f6f4 v[52:55], v[16:23], v[232:239], v[52:55]
	v_mfma_f32_16x16x128_f8f6f4 v[48:51], v[24:31], v[232:239], v[48:51]
	v_mfma_f32_16x16x128_f8f6f4 v[36:39], v[16:23], v[240:247], v[36:39]
	v_mfma_f32_16x16x128_f8f6f4 v[32:35], v[24:31], v[240:247], v[32:35]
	s_setprio 0
	s_barrier
	s_add_i32 s60, s60, 2
	s_add_u32 s26, s26, 0x100
	s_addc_u32 s27, s27, 0
	s_cmp_gt_u32 s60, 5
	s_cbranch_scc1 .LBB0_820

.LBB0_838:
	s_add_u32 s36, s4, 0x100
	s_addc_u32 s37, s5, 0
	v_mov_b32_e32 v129, v137
	v_mov_b32_e32 v131, v137
	s_add_u32 s57, s6, 0x100
	v_mov_b32_e32 v0, 0
	v_mov_b32_e32 v143, v137
	v_mov_b32_e32 v145, v137
	v_lshl_add_u64 v[146:147], s[22:23], 0, v[130:131]
	v_lshl_add_u64 v[148:149], s[22:23], 0, v[128:129]
	s_addc_u32 s60, s7, 0
	s_mov_b32 s61, -2
	s_mov_b64 s[4:5], 0
	v_mov_b32_e32 v1, v0
	v_mov_b32_e32 v2, v0
	v_mov_b32_e32 v3, v0
	v_mov_b32_e32 v4, v0
	v_mov_b32_e32 v5, v0
	v_mov_b32_e32 v6, v0
	v_mov_b32_e32 v7, v0
	v_mov_b32_e32 v16, v0
	v_mov_b32_e32 v17, v0
	v_mov_b32_e32 v18, v0
	v_mov_b32_e32 v19, v0
	v_mov_b32_e32 v20, v0
	v_mov_b32_e32 v21, v0
	v_mov_b32_e32 v22, v0
	v_mov_b32_e32 v23, v0
	v_mov_b32_e32 v32, v0
	v_mov_b32_e32 v33, v0
	v_mov_b32_e32 v34, v0
	v_mov_b32_e32 v35, v0
	v_mov_b32_e32 v36, v0
	v_mov_b32_e32 v37, v0
	v_mov_b32_e32 v38, v0
	v_mov_b32_e32 v39, v0
	v_mov_b32_e32 v48, v0
	v_mov_b32_e32 v49, v0
	v_mov_b32_e32 v50, v0
	v_mov_b32_e32 v51, v0
	v_mov_b32_e32 v52, v0
	v_mov_b32_e32 v53, v0
	v_mov_b32_e32 v54, v0
	v_mov_b32_e32 v55, v0
	v_mov_b32_e32 v8, v0
	v_mov_b32_e32 v9, v0
	v_mov_b32_e32 v10, v0
	v_mov_b32_e32 v11, v0
	v_mov_b32_e32 v12, v0
	v_mov_b32_e32 v13, v0
	v_mov_b32_e32 v14, v0
	v_mov_b32_e32 v15, v0
	v_mov_b32_e32 v24, v0
	v_mov_b32_e32 v25, v0
	v_mov_b32_e32 v26, v0
	v_mov_b32_e32 v27, v0
	v_mov_b32_e32 v28, v0
	v_mov_b32_e32 v29, v0
	v_mov_b32_e32 v30, v0
	v_mov_b32_e32 v31, v0
	v_mov_b32_e32 v40, v0
	v_mov_b32_e32 v41, v0
	v_mov_b32_e32 v42, v0
	v_mov_b32_e32 v43, v0
	v_mov_b32_e32 v44, v0
	v_mov_b32_e32 v45, v0
	v_mov_b32_e32 v46, v0
	v_mov_b32_e32 v47, v0
	v_mov_b32_e32 v56, v0
	v_mov_b32_e32 v57, v0
	v_mov_b32_e32 v58, v0
	v_mov_b32_e32 v59, v0
	v_mov_b32_e32 v60, v0
	v_mov_b32_e32 v61, v0
	v_mov_b32_e32 v62, v0
	v_mov_b32_e32 v63, v0
	v_mov_b32_e32 v64, v0
	v_mov_b32_e32 v65, v0
	v_mov_b32_e32 v66, v0
	v_mov_b32_e32 v67, v0
	v_mov_b32_e32 v68, v0
	v_mov_b32_e32 v69, v0
	v_mov_b32_e32 v70, v0
	v_mov_b32_e32 v71, v0
	v_mov_b32_e32 v80, v0
	v_mov_b32_e32 v81, v0
	v_mov_b32_e32 v82, v0
	v_mov_b32_e32 v83, v0
	v_mov_b32_e32 v84, v0
	v_mov_b32_e32 v85, v0
	v_mov_b32_e32 v86, v0
	v_mov_b32_e32 v87, v0
	v_mov_b32_e32 v96, v0
	v_mov_b32_e32 v97, v0
	v_mov_b32_e32 v98, v0
	v_mov_b32_e32 v99, v0
	v_mov_b32_e32 v100, v0
	v_mov_b32_e32 v101, v0
	v_mov_b32_e32 v102, v0
	v_mov_b32_e32 v103, v0
	v_mov_b32_e32 v112, v0
	v_mov_b32_e32 v113, v0
	v_mov_b32_e32 v114, v0
	v_mov_b32_e32 v115, v0
	v_mov_b32_e32 v116, v0
	v_mov_b32_e32 v117, v0
	v_mov_b32_e32 v118, v0
	v_mov_b32_e32 v119, v0
	v_mov_b32_e32 v72, v0
	v_mov_b32_e32 v73, v0
	v_mov_b32_e32 v74, v0
	v_mov_b32_e32 v75, v0
	v_mov_b32_e32 v76, v0
	v_mov_b32_e32 v77, v0
	v_mov_b32_e32 v78, v0
	v_mov_b32_e32 v79, v0
	v_mov_b32_e32 v88, v0
	v_mov_b32_e32 v89, v0
	v_mov_b32_e32 v90, v0
	v_mov_b32_e32 v91, v0
	v_mov_b32_e32 v92, v0
	v_mov_b32_e32 v93, v0
	v_mov_b32_e32 v94, v0
	v_mov_b32_e32 v95, v0
	v_mov_b32_e32 v104, v0
	v_mov_b32_e32 v105, v0
	v_mov_b32_e32 v106, v0
	v_mov_b32_e32 v107, v0
	v_mov_b32_e32 v108, v0
	v_mov_b32_e32 v109, v0
	v_mov_b32_e32 v110, v0
	v_mov_b32_e32 v111, v0
	v_mov_b32_e32 v120, v0
	v_mov_b32_e32 v121, v0
	v_mov_b32_e32 v122, v0
	v_mov_b32_e32 v123, v0
	v_mov_b32_e32 v124, v0
	v_mov_b32_e32 v125, v0
	v_mov_b32_e32 v126, v0
	v_mov_b32_e32 v127, v0
	v_add_u32_e32 v252, 0x10000, v159
	v_add_u32_e32 v253, 0x10000, v160
	s_branch .LBB0_840
.LBB0_839:
	s_add_u32 s6, s10, s4
	s_addc_u32 s7, s11, s5
	s_add_u32 s34, s6, 0xe000100
	s_addc_u32 s35, s7, 0
	ds_read_b128 v[166:169], v252
	ds_read_b128 v[170:173], v253
	s_and_b64 s[6:7], s[30:31], exec
	ds_read_b128 v[174:177], v252 offset:2048
	ds_read_b128 v[178:181], v253 offset:2048
	s_cselect_b32 s7, s1, s35
	s_cselect_b32 s6, s0, s34
	s_add_u32 s62, s36, s4
	ds_read_b128 v[182:185], v252 offset:16384
	ds_read_b128 v[186:189], v253 offset:16384
	s_addc_u32 s63, s37, s5
	ds_read_b128 v[190:193], v252 offset:18432
	ds_read_b128 v[194:197], v253 offset:18432
	s_and_b64 s[34:35], s[30:31], exec
	s_cselect_b32 s35, s27, s63
	s_cselect_b32 s34, s26, s62
	s_add_u32 s62, s57, s4
	s_addc_u32 s63, s60, s5
	s_and_b64 s[30:31], s[30:31], exec
	s_cselect_b32 s31, s29, s63
	s_cselect_b32 s30, s28, s62
	v_lshl_add_u64 v[232:233], v[148:149], 0, s[4:5]
	s_add_i32 m0, s40, 0xc000
	ds_read_b128 v[200:203], v161
	ds_read_b128 v[204:207], v161 offset:1024
	ds_read_b128 v[208:211], v161 offset:2048
	ds_read_b128 v[212:215], v161 offset:3072
	ds_read_b128 v[216:219], v161 offset:4096
	ds_read_b128 v[220:223], v161 offset:5120
	ds_read_b128 v[224:227], v161 offset:6144
	ds_read_b128 v[228:231], v161 offset:7168
	global_load_lds_dwordx4 v[232:233], off
	v_lshl_add_u64 v[232:233], v[146:147], 0, s[4:5]
	s_add_i32 m0, s40, 0xe000
	s_nop 0
	global_load_lds_dwordx4 v[232:233], off
	s_waitcnt vmcnt(8)
	s_waitcnt lgkmcnt(0)
	s_barrier
	s_setprio 1
	s_waitcnt lgkmcnt(0)
	v_mfma_f32_16x16x32_bf16 v[124:127], v[166:169], v[200:203], v[124:127]
	v_mfma_f32_16x16x32_bf16 v[120:123], v[174:177], v[200:203], v[120:123]
	v_mfma_f32_16x16x32_bf16 v[108:111], v[166:169], v[208:211], v[108:111]
	v_mfma_f32_16x16x32_bf16 v[104:107], v[174:177], v[208:211], v[104:107]
	v_mfma_f32_16x16x32_bf16 v[92:95], v[166:169], v[216:219], v[92:95]
	v_mfma_f32_16x16x32_bf16 v[88:91], v[174:177], v[216:219], v[88:91]
	v_mfma_f32_16x16x32_bf16 v[76:79], v[166:169], v[224:227], v[76:79]
	v_mfma_f32_16x16x32_bf16 v[72:75], v[174:177], v[224:227], v[72:75]
	v_mfma_f32_16x16x32_bf16 v[124:127], v[170:173], v[204:207], v[124:127]
	v_mfma_f32_16x16x32_bf16 v[120:123], v[178:181], v[204:207], v[120:123]
	v_mfma_f32_16x16x32_bf16 v[108:111], v[170:173], v[212:215], v[108:111]
	v_mfma_f32_16x16x32_bf16 v[104:107], v[178:181], v[212:215], v[104:107]
	v_mfma_f32_16x16x32_bf16 v[92:95], v[170:173], v[220:223], v[92:95]
	v_mfma_f32_16x16x32_bf16 v[88:91], v[178:181], v[220:223], v[88:91]
	v_mfma_f32_16x16x32_bf16 v[76:79], v[170:173], v[228:231], v[76:79]
	v_mfma_f32_16x16x32_bf16 v[72:75], v[178:181], v[228:231], v[72:75]
	v_mfma_f32_16x16x32_bf16 v[116:119], v[182:185], v[200:203], v[116:119]
	v_mfma_f32_16x16x32_bf16 v[112:115], v[190:193], v[200:203], v[112:115]
	v_mfma_f32_16x16x32_bf16 v[100:103], v[182:185], v[208:211], v[100:103]
	v_mfma_f32_16x16x32_bf16 v[96:99], v[190:193], v[208:211], v[96:99]
	v_mfma_f32_16x16x32_bf16 v[84:87], v[182:185], v[216:219], v[84:87]
	v_mfma_f32_16x16x32_bf16 v[80:83], v[190:193], v[216:219], v[80:83]
	v_mfma_f32_16x16x32_bf16 v[68:71], v[182:185], v[224:227], v[68:71]
	v_mfma_f32_16x16x32_bf16 v[64:67], v[190:193], v[224:227], v[64:67]
	v_mfma_f32_16x16x32_bf16 v[116:119], v[186:189], v[204:207], v[116:119]
	v_mfma_f32_16x16x32_bf16 v[112:115], v[194:197], v[204:207], v[112:115]
	v_mfma_f32_16x16x32_bf16 v[100:103], v[186:189], v[212:215], v[100:103]
	v_mfma_f32_16x16x32_bf16 v[96:99], v[194:197], v[212:215], v[96:99]
	v_mfma_f32_16x16x32_bf16 v[84:87], v[186:189], v[220:223], v[84:87]
	v_mfma_f32_16x16x32_bf16 v[80:83], v[194:197], v[220:223], v[80:83]
	v_mfma_f32_16x16x32_bf16 v[68:71], v[186:189], v[228:231], v[68:71]
	v_mfma_f32_16x16x32_bf16 v[64:67], v[194:197], v[228:231], v[64:67]
	s_setprio 0
	s_barrier
	s_add_i32 s62, s49, s39
	v_lshl_add_u64 v[232:233], s[34:35], 0, v[132:133]
	s_mov_b32 m0, s62
	ds_read_b128 v[200:203], v161 offset:16384
	ds_read_b128 v[204:207], v161 offset:17408
	ds_read_b128 v[208:211], v161 offset:18432
	ds_read_b128 v[212:215], v161 offset:19456
	ds_read_b128 v[216:219], v161 offset:20480
	ds_read_b128 v[220:223], v161 offset:21504
	ds_read_b128 v[224:227], v161 offset:22528
	ds_read_b128 v[228:231], v161 offset:23552
	global_load_lds_dwordx4 v[232:233], off
	v_lshl_add_u64 v[234:235], s[34:35], 0, v[134:135]
	s_add_i32 m0, s62, 0x2000
	s_add_i32 s34, s51, s39
	global_load_lds_dwordx4 v[234:235], off
	v_lshl_add_u64 v[236:237], s[30:31], 0, v[132:133]
	s_mov_b32 m0, s34
	v_lshl_add_u64 v[238:239], s[30:31], 0, v[134:135]
	global_load_lds_dwordx4 v[236:237], off
	s_add_i32 m0, s34, 0x2000
	v_mov_b32_e32 v139, v137
	global_load_lds_dwordx4 v[238:239], off
	s_mov_b32 m0, s40
	v_lshl_add_u64 v[240:241], s[6:7], 0, v[136:137]
	global_load_lds_dwordx4 v136, s[6:7]
	s_mov_b32 m0, s41
	v_lshl_add_u64 v[242:243], s[6:7], 0, v[138:139]
	global_load_lds_dwordx4 v138, s[6:7]
	s_waitcnt vmcnt(8)
	s_waitcnt lgkmcnt(0)
	s_barrier
	s_setprio 1
	s_waitcnt lgkmcnt(0)
	v_mfma_f32_16x16x32_bf16 v[60:63], v[166:169], v[200:203], v[60:63]
	v_mfma_f32_16x16x32_bf16 v[56:59], v[174:177], v[200:203], v[56:59]
	v_mfma_f32_16x16x32_bf16 v[44:47], v[166:169], v[208:211], v[44:47]
	v_mfma_f32_16x16x32_bf16 v[40:43], v[174:177], v[208:211], v[40:43]
	v_mfma_f32_16x16x32_bf16 v[28:31], v[166:169], v[216:219], v[28:31]
	v_mfma_f32_16x16x32_bf16 v[24:27], v[174:177], v[216:219], v[24:27]
	v_mfma_f32_16x16x32_bf16 v[12:15], v[166:169], v[224:227], v[12:15]
	v_mfma_f32_16x16x32_bf16 v[8:11], v[174:177], v[224:227], v[8:11]
	v_mfma_f32_16x16x32_bf16 v[60:63], v[170:173], v[204:207], v[60:63]
	v_mfma_f32_16x16x32_bf16 v[56:59], v[178:181], v[204:207], v[56:59]
	v_mfma_f32_16x16x32_bf16 v[44:47], v[170:173], v[212:215], v[44:47]
	v_mfma_f32_16x16x32_bf16 v[40:43], v[178:181], v[212:215], v[40:43]
	v_mfma_f32_16x16x32_bf16 v[28:31], v[170:173], v[220:223], v[28:31]
	v_mfma_f32_16x16x32_bf16 v[24:27], v[178:181], v[220:223], v[24:27]
	v_mfma_f32_16x16x32_bf16 v[12:15], v[170:173], v[228:231], v[12:15]
	v_mfma_f32_16x16x32_bf16 v[8:11], v[178:181], v[228:231], v[8:11]
	v_mfma_f32_16x16x32_bf16 v[52:55], v[182:185], v[200:203], v[52:55]
	v_mfma_f32_16x16x32_bf16 v[48:51], v[190:193], v[200:203], v[48:51]
	v_mfma_f32_16x16x32_bf16 v[36:39], v[182:185], v[208:211], v[36:39]
	v_mfma_f32_16x16x32_bf16 v[32:35], v[190:193], v[208:211], v[32:35]
	v_mfma_f32_16x16x32_bf16 v[20:23], v[182:185], v[216:219], v[20:23]
	v_mfma_f32_16x16x32_bf16 v[16:19], v[190:193], v[216:219], v[16:19]
	v_mfma_f32_16x16x32_bf16 v[4:7], v[182:185], v[224:227], v[4:7]
	v_mfma_f32_16x16x32_bf16 v[0:3], v[190:193], v[224:227], v[0:3]
	v_mfma_f32_16x16x32_bf16 v[52:55], v[186:189], v[204:207], v[52:55]
	v_mfma_f32_16x16x32_bf16 v[48:51], v[194:197], v[204:207], v[48:51]
	v_mfma_f32_16x16x32_bf16 v[36:39], v[186:189], v[212:215], v[36:39]
	v_mfma_f32_16x16x32_bf16 v[32:35], v[194:197], v[212:215], v[32:35]
	v_mfma_f32_16x16x32_bf16 v[20:23], v[186:189], v[220:223], v[20:23]
	v_mfma_f32_16x16x32_bf16 v[16:19], v[194:197], v[220:223], v[16:19]
	v_mfma_f32_16x16x32_bf16 v[4:7], v[186:189], v[228:231], v[4:7]
	v_mfma_f32_16x16x32_bf16 v[0:3], v[194:197], v[228:231], v[0:3]
	s_setprio 0
	s_barrier
	s_add_i32 s30, 0, 0x18000
	ds_read_b128 v[166:169], v252 offset:32768
	ds_read_b128 v[170:173], v253 offset:32768
	s_add_i32 s31, 0, 0x1c000
	ds_read_b128 v[174:177], v252 offset:34816
	ds_read_b128 v[178:181], v253 offset:34816
	ds_read_b128 v[182:185], v252 offset:49152
	ds_read_b128 v[186:189], v253 offset:49152
	ds_read_b128 v[190:193], v252 offset:51200
	ds_read_b128 v[194:197], v253 offset:51200
	s_mov_b32 m0, s42
	v_lshl_add_u64 v[152:153], s[6:7], 0, v[152:153]
	ds_read_b128 v[200:203], v161 offset:32768
	ds_read_b128 v[204:207], v161 offset:33792
	ds_read_b128 v[208:211], v161 offset:34816
	ds_read_b128 v[212:215], v161 offset:35840
	ds_read_b128 v[216:219], v161 offset:36864
	ds_read_b128 v[220:223], v161 offset:37888
	ds_read_b128 v[224:227], v161 offset:38912
	ds_read_b128 v[228:231], v161 offset:39936
	global_load_lds_dwordx4 v[152:153], off
	v_lshl_add_u64 v[150:151], s[6:7], 0, v[150:151]
	s_mov_b32 m0, s43
	s_nop 0
	global_load_lds_dwordx4 v[150:151], off
	s_waitcnt vmcnt(8)
	s_waitcnt lgkmcnt(0)
	s_barrier
	s_setprio 1
	s_waitcnt lgkmcnt(0)
	v_mfma_f32_16x16x32_bf16 v[124:127], v[166:169], v[200:203], v[124:127]
	v_mfma_f32_16x16x32_bf16 v[120:123], v[174:177], v[200:203], v[120:123]
	v_mfma_f32_16x16x32_bf16 v[108:111], v[166:169], v[208:211], v[108:111]
	v_mfma_f32_16x16x32_bf16 v[104:107], v[174:177], v[208:211], v[104:107]
	v_mfma_f32_16x16x32_bf16 v[92:95], v[166:169], v[216:219], v[92:95]
	v_mfma_f32_16x16x32_bf16 v[88:91], v[174:177], v[216:219], v[88:91]
	v_mfma_f32_16x16x32_bf16 v[76:79], v[166:169], v[224:227], v[76:79]
	v_mfma_f32_16x16x32_bf16 v[72:75], v[174:177], v[224:227], v[72:75]
	v_mfma_f32_16x16x32_bf16 v[124:127], v[170:173], v[204:207], v[124:127]
	v_mfma_f32_16x16x32_bf16 v[120:123], v[178:181], v[204:207], v[120:123]
	v_mfma_f32_16x16x32_bf16 v[108:111], v[170:173], v[212:215], v[108:111]
	v_mfma_f32_16x16x32_bf16 v[104:107], v[178:181], v[212:215], v[104:107]
	v_mfma_f32_16x16x32_bf16 v[92:95], v[170:173], v[220:223], v[92:95]
	v_mfma_f32_16x16x32_bf16 v[88:91], v[178:181], v[220:223], v[88:91]
	v_mfma_f32_16x16x32_bf16 v[76:79], v[170:173], v[228:231], v[76:79]
	v_mfma_f32_16x16x32_bf16 v[72:75], v[178:181], v[228:231], v[72:75]
	v_mfma_f32_16x16x32_bf16 v[116:119], v[182:185], v[200:203], v[116:119]
	v_mfma_f32_16x16x32_bf16 v[112:115], v[190:193], v[200:203], v[112:115]
	v_mfma_f32_16x16x32_bf16 v[100:103], v[182:185], v[208:211], v[100:103]
	v_mfma_f32_16x16x32_bf16 v[96:99], v[190:193], v[208:211], v[96:99]
	v_mfma_f32_16x16x32_bf16 v[84:87], v[182:185], v[216:219], v[84:87]
	v_mfma_f32_16x16x32_bf16 v[80:83], v[190:193], v[216:219], v[80:83]
	v_mfma_f32_16x16x32_bf16 v[68:71], v[182:185], v[224:227], v[68:71]
	v_mfma_f32_16x16x32_bf16 v[64:67], v[190:193], v[224:227], v[64:67]
	v_mfma_f32_16x16x32_bf16 v[116:119], v[186:189], v[204:207], v[116:119]
	v_mfma_f32_16x16x32_bf16 v[112:115], v[194:197], v[204:207], v[112:115]
	v_mfma_f32_16x16x32_bf16 v[100:103], v[186:189], v[212:215], v[100:103]
	v_mfma_f32_16x16x32_bf16 v[96:99], v[194:197], v[212:215], v[96:99]
	v_mfma_f32_16x16x32_bf16 v[84:87], v[186:189], v[220:223], v[84:87]
	v_mfma_f32_16x16x32_bf16 v[80:83], v[194:197], v[220:223], v[80:83]
	v_mfma_f32_16x16x32_bf16 v[68:71], v[186:189], v[228:231], v[68:71]
	v_mfma_f32_16x16x32_bf16 v[64:67], v[194:197], v[228:231], v[64:67]
	s_setprio 0
	s_barrier
	s_add_i32 s6, s30, s39
	v_lshl_add_u64 v[228:229], v[232:233], 0, s[20:21]
	s_mov_b32 m0, s6
	ds_read_b128 v[150:153], v161 offset:49152
	ds_read_b128 v[200:203], v161 offset:50176
	ds_read_b128 v[204:207], v161 offset:51200
	ds_read_b128 v[208:211], v161 offset:52224
	ds_read_b128 v[212:215], v161 offset:53248
	ds_read_b128 v[216:219], v161 offset:54272
	ds_read_b128 v[220:223], v161 offset:55296
	ds_read_b128 v[224:227], v161 offset:56320
	global_load_lds_dwordx4 v[228:229], off
	v_lshl_add_u64 v[228:229], v[234:235], 0, s[20:21]
	s_add_i32 m0, s6, 0x2000
	s_add_i32 s6, s31, s39
	global_load_lds_dwordx4 v[228:229], off
	v_lshl_add_u64 v[228:229], v[236:237], 0, s[20:21]
	s_mov_b32 m0, s6
	s_nop 0
	global_load_lds_dwordx4 v[228:229], off
	v_lshl_add_u64 v[228:229], v[238:239], 0, s[20:21]
	s_add_i32 m0, s6, 0x2000
	s_nop 0
	global_load_lds_dwordx4 v[228:229], off
	v_lshl_add_u64 v[228:229], v[240:241], 0, s[20:21]
	s_mov_b32 m0, s47
	s_nop 0
	global_load_lds_dwordx4 v[228:229], off
	v_lshl_add_u64 v[228:229], v[242:243], 0, s[20:21]
	s_mov_b32 m0, s48
	s_nop 0
	global_load_lds_dwordx4 v[228:229], off
	s_waitcnt vmcnt(8)
	s_waitcnt lgkmcnt(0)
	s_barrier
	s_setprio 1
	s_waitcnt lgkmcnt(0)
	v_mfma_f32_16x16x32_bf16 v[60:63], v[166:169], v[150:153], v[60:63]
	v_mfma_f32_16x16x32_bf16 v[56:59], v[174:177], v[150:153], v[56:59]
	v_mfma_f32_16x16x32_bf16 v[44:47], v[166:169], v[204:207], v[44:47]
	v_mfma_f32_16x16x32_bf16 v[40:43], v[174:177], v[204:207], v[40:43]
	v_mfma_f32_16x16x32_bf16 v[28:31], v[166:169], v[212:215], v[28:31]
	v_mfma_f32_16x16x32_bf16 v[24:27], v[174:177], v[212:215], v[24:27]
	v_mfma_f32_16x16x32_bf16 v[12:15], v[166:169], v[220:223], v[12:15]
	v_mfma_f32_16x16x32_bf16 v[8:11], v[174:177], v[220:223], v[8:11]
	v_mfma_f32_16x16x32_bf16 v[60:63], v[170:173], v[200:203], v[60:63]
	v_mfma_f32_16x16x32_bf16 v[56:59], v[178:181], v[200:203], v[56:59]
	v_mfma_f32_16x16x32_bf16 v[44:47], v[170:173], v[208:211], v[44:47]
	v_mfma_f32_16x16x32_bf16 v[40:43], v[178:181], v[208:211], v[40:43]
	v_mfma_f32_16x16x32_bf16 v[28:31], v[170:173], v[216:219], v[28:31]
	v_mfma_f32_16x16x32_bf16 v[24:27], v[178:181], v[216:219], v[24:27]
	v_mfma_f32_16x16x32_bf16 v[12:15], v[170:173], v[224:227], v[12:15]
	v_mfma_f32_16x16x32_bf16 v[8:11], v[178:181], v[224:227], v[8:11]
	v_mfma_f32_16x16x32_bf16 v[52:55], v[182:185], v[150:153], v[52:55]
	v_mfma_f32_16x16x32_bf16 v[48:51], v[190:193], v[150:153], v[48:51]
	v_mfma_f32_16x16x32_bf16 v[36:39], v[182:185], v[204:207], v[36:39]
	v_mfma_f32_16x16x32_bf16 v[32:35], v[190:193], v[204:207], v[32:35]
	v_mfma_f32_16x16x32_bf16 v[20:23], v[182:185], v[212:215], v[20:23]
	v_mfma_f32_16x16x32_bf16 v[16:19], v[190:193], v[212:215], v[16:19]
	v_mfma_f32_16x16x32_bf16 v[4:7], v[182:185], v[220:223], v[4:7]
	v_mfma_f32_16x16x32_bf16 v[0:3], v[190:193], v[220:223], v[0:3]
	v_mfma_f32_16x16x32_bf16 v[52:55], v[186:189], v[200:203], v[52:55]
	v_mfma_f32_16x16x32_bf16 v[48:51], v[194:197], v[200:203], v[48:51]
	v_mfma_f32_16x16x32_bf16 v[36:39], v[186:189], v[208:211], v[36:39]
	v_mfma_f32_16x16x32_bf16 v[32:35], v[194:197], v[208:211], v[32:35]
	v_mfma_f32_16x16x32_bf16 v[20:23], v[186:189], v[216:219], v[20:23]
	v_mfma_f32_16x16x32_bf16 v[16:19], v[194:197], v[216:219], v[16:19]
	v_mfma_f32_16x16x32_bf16 v[4:7], v[186:189], v[224:227], v[4:7]
	v_mfma_f32_16x16x32_bf16 v[0:3], v[194:197], v[224:227], v[0:3]
	s_setprio 0
	s_barrier
	s_add_i32 s61, s61, 2
	s_add_u32 s4, s4, 0x100
	s_addc_u32 s5, s5, 0
	s_cmp_gt_u32 s61, 13
	s_cbranch_scc1 .LBB0_842

.LBB0_1548:
	s_add_u32 s58, s24, 0x100
	s_addc_u32 s59, s25, 0
	v_mov_b32_e32 v169, v165
	v_mov_b32_e32 v171, v165
	s_add_u32 s60, s26, 0x100
	v_mov_b32_e32 v32, 0
	v_mov_b32_e32 v175, v165
	v_mov_b32_e32 v177, v165
	v_lshl_add_u64 v[178:179], s[14:15], 0, v[170:171]
	v_lshl_add_u64 v[180:181], s[14:15], 0, v[168:169]
	s_addc_u32 s61, s27, 0
	s_mov_b32 s62, -2
	s_mov_b64 s[24:25], 0
	v_mov_b32_e32 v33, v32
	v_mov_b32_e32 v34, v32
	v_mov_b32_e32 v35, v32
	v_mov_b32_e32 v36, v32
	v_mov_b32_e32 v37, v32
	v_mov_b32_e32 v38, v32
	v_mov_b32_e32 v39, v32
	v_mov_b32_e32 v44, v32
	v_mov_b32_e32 v45, v32
	v_mov_b32_e32 v46, v32
	v_mov_b32_e32 v47, v32
	v_mov_b32_e32 v52, v32
	v_mov_b32_e32 v53, v32
	v_mov_b32_e32 v54, v32
	v_mov_b32_e32 v55, v32
	v_mov_b32_e32 v64, v32
	v_mov_b32_e32 v65, v32
	v_mov_b32_e32 v66, v32
	v_mov_b32_e32 v67, v32
	v_mov_b32_e32 v68, v32
	v_mov_b32_e32 v69, v32
	v_mov_b32_e32 v70, v32
	v_mov_b32_e32 v71, v32
	v_mov_b32_e32 v76, v32
	v_mov_b32_e32 v77, v32
	v_mov_b32_e32 v78, v32
	v_mov_b32_e32 v79, v32
	v_mov_b32_e32 v84, v32
	v_mov_b32_e32 v85, v32
	v_mov_b32_e32 v86, v32
	v_mov_b32_e32 v87, v32
	v_mov_b32_e32 v40, v32
	v_mov_b32_e32 v41, v32
	v_mov_b32_e32 v42, v32
	v_mov_b32_e32 v43, v32
	v_mov_b32_e32 v48, v32
	v_mov_b32_e32 v49, v32
	v_mov_b32_e32 v50, v32
	v_mov_b32_e32 v51, v32
	v_mov_b32_e32 v56, v32
	v_mov_b32_e32 v57, v32
	v_mov_b32_e32 v58, v32
	v_mov_b32_e32 v59, v32
	v_mov_b32_e32 v60, v32
	v_mov_b32_e32 v61, v32
	v_mov_b32_e32 v62, v32
	v_mov_b32_e32 v63, v32
	v_mov_b32_e32 v72, v32
	v_mov_b32_e32 v73, v32
	v_mov_b32_e32 v74, v32
	v_mov_b32_e32 v75, v32
	v_mov_b32_e32 v80, v32
	v_mov_b32_e32 v81, v32
	v_mov_b32_e32 v82, v32
	v_mov_b32_e32 v83, v32
	v_mov_b32_e32 v88, v32
	v_mov_b32_e32 v89, v32
	v_mov_b32_e32 v90, v32
	v_mov_b32_e32 v91, v32
	v_mov_b32_e32 v92, v32
	v_mov_b32_e32 v93, v32
	v_mov_b32_e32 v94, v32
	v_mov_b32_e32 v95, v32
	v_mov_b32_e32 v96, v32
	v_mov_b32_e32 v97, v32
	v_mov_b32_e32 v98, v32
	v_mov_b32_e32 v99, v32
	v_mov_b32_e32 v100, v32
	v_mov_b32_e32 v101, v32
	v_mov_b32_e32 v102, v32
	v_mov_b32_e32 v103, v32
	v_mov_b32_e32 v108, v32
	v_mov_b32_e32 v109, v32
	v_mov_b32_e32 v110, v32
	v_mov_b32_e32 v111, v32
	s_waitcnt vmcnt(0)
	v_mov_b32_e32 v116, v32
	v_mov_b32_e32 v117, v32
	v_mov_b32_e32 v118, v32
	v_mov_b32_e32 v119, v32
	v_mov_b32_e32 v128, v32
	v_mov_b32_e32 v129, v32
	v_mov_b32_e32 v130, v32
	v_mov_b32_e32 v131, v32
	v_mov_b32_e32 v132, v32
	v_mov_b32_e32 v133, v32
	v_mov_b32_e32 v134, v32
	v_mov_b32_e32 v135, v32
	v_mov_b32_e32 v140, v32
	v_mov_b32_e32 v141, v32
	v_mov_b32_e32 v142, v32
	v_mov_b32_e32 v143, v32
	v_mov_b32_e32 v148, v32
	v_mov_b32_e32 v149, v32
	v_mov_b32_e32 v150, v32
	v_mov_b32_e32 v151, v32
	v_mov_b32_e32 v104, v32
	v_mov_b32_e32 v105, v32
	v_mov_b32_e32 v106, v32
	v_mov_b32_e32 v107, v32
	v_mov_b32_e32 v112, v32
	v_mov_b32_e32 v113, v32
	v_mov_b32_e32 v114, v32
	v_mov_b32_e32 v115, v32
	v_mov_b32_e32 v120, v32
	v_mov_b32_e32 v121, v32
	v_mov_b32_e32 v122, v32
	v_mov_b32_e32 v123, v32
	v_mov_b32_e32 v124, v32
	v_mov_b32_e32 v125, v32
	v_mov_b32_e32 v126, v32
	v_mov_b32_e32 v127, v32
	v_mov_b32_e32 v136, v32
	v_mov_b32_e32 v137, v32
	v_mov_b32_e32 v138, v32
	v_mov_b32_e32 v139, v32
	v_mov_b32_e32 v144, v32
	v_mov_b32_e32 v145, v32
	v_mov_b32_e32 v146, v32
	v_mov_b32_e32 v147, v32
	v_mov_b32_e32 v152, v32
	v_mov_b32_e32 v153, v32
	v_mov_b32_e32 v154, v32
	v_mov_b32_e32 v155, v32
	v_mov_b32_e32 v156, v32
	v_mov_b32_e32 v157, v32
	v_mov_b32_e32 v158, v32
	v_mov_b32_e32 v159, v32
	v_add_u32_e32 v252, 0x10000, v204
	v_add_u32_e32 v253, 0x10000, v205
	s_branch .LBB0_1550
.LBB0_1549:
	s_add_u32 s26, s4, s24
	s_addc_u32 s27, s5, s25
	s_add_u32 s28, s26, 0x28000100
	s_addc_u32 s29, s27, 0
	ds_read_b128 v[24:27], v252
	ds_read_b128 v[28:31], v253
	s_and_b64 s[26:27], s[30:31], exec
	ds_read_b128 v[16:19], v252 offset:2048
	ds_read_b128 v[20:23], v253 offset:2048
	s_cselect_b32 s27, s7, s29
	s_cselect_b32 s26, s6, s28
	s_add_u32 s63, s58, s24
	ds_read_b128 v[8:11], v252 offset:16384
	ds_read_b128 v[12:15], v253 offset:16384
	s_addc_u32 s64, s59, s25
	ds_read_b128 v[0:3], v252 offset:18432
	ds_read_b128 v[4:7], v253 offset:18432
	s_and_b64 s[28:29], s[30:31], exec
	s_cselect_b32 s29, s21, s64
	s_cselect_b32 s28, s20, s63
	s_add_u32 s63, s60, s24
	s_addc_u32 s64, s61, s25
	s_and_b64 s[30:31], s[30:31], exec
	s_cselect_b32 s31, s23, s64
	s_cselect_b32 s30, s22, s63
	v_lshl_add_u64 v[194:195], v[180:181], 0, s[24:25]
	s_add_i32 m0, s35, 0xc000
	ds_read_b128 v[186:189], v206
	ds_read_b128 v[214:217], v206 offset:2048
	ds_read_b128 v[190:193], v207
	ds_read_b128 v[218:221], v207 offset:2048
	ds_read_b128 v[222:225], v206 offset:4096
	ds_read_b128 v[230:233], v206 offset:6144
	ds_read_b128 v[226:229], v207 offset:4096
	ds_read_b128 v[234:237], v207 offset:6144
	global_load_lds_dwordx4 v[194:195], off
	v_lshl_add_u64 v[194:195], v[178:179], 0, s[24:25]
	s_add_i32 m0, s35, 0xe000
	s_nop 0
	global_load_lds_dwordx4 v[194:195], off
	s_waitcnt vmcnt(8)
	s_waitcnt lgkmcnt(0)
	s_barrier
	s_setprio 1
	s_waitcnt lgkmcnt(0)
	v_mfma_f32_16x16x128_f8f6f4 v[156:159], v[24:31], v[186:193], v[156:159]
	v_mfma_f32_16x16x128_f8f6f4 v[152:155], v[16:23], v[186:193], v[152:155]
	v_mfma_f32_16x16x128_f8f6f4 v[144:147], v[24:31], v[214:221], v[144:147]
	v_mfma_f32_16x16x128_f8f6f4 v[136:139], v[16:23], v[214:221], v[136:139]
	v_mfma_f32_16x16x128_f8f6f4 v[124:127], v[24:31], v[222:229], v[124:127]
	v_mfma_f32_16x16x128_f8f6f4 v[120:123], v[16:23], v[222:229], v[120:123]
	v_mfma_f32_16x16x128_f8f6f4 v[112:115], v[24:31], v[230:237], v[112:115]
	v_mfma_f32_16x16x128_f8f6f4 v[104:107], v[16:23], v[230:237], v[104:107]
	v_mfma_f32_16x16x128_f8f6f4 v[148:151], v[8:15], v[186:193], v[148:151]
	v_mfma_f32_16x16x128_f8f6f4 v[140:143], v[0:7], v[186:193], v[140:143]
	v_mfma_f32_16x16x128_f8f6f4 v[132:135], v[8:15], v[214:221], v[132:135]
	v_mfma_f32_16x16x128_f8f6f4 v[128:131], v[0:7], v[214:221], v[128:131]
	v_mfma_f32_16x16x128_f8f6f4 v[116:119], v[8:15], v[222:229], v[116:119]
	v_mfma_f32_16x16x128_f8f6f4 v[108:111], v[0:7], v[222:229], v[108:111]
	v_mfma_f32_16x16x128_f8f6f4 v[100:103], v[8:15], v[230:237], v[100:103]
	v_mfma_f32_16x16x128_f8f6f4 v[96:99], v[0:7], v[230:237], v[96:99]
	s_setprio 0
	s_barrier
	s_add_i32 s63, s46, s34
	v_lshl_add_u64 v[186:187], s[28:29], 0, v[160:161]
	s_mov_b32 m0, s63
	ds_read_b128 v[214:217], v206 offset:16384
	ds_read_b128 v[222:225], v206 offset:18432
	ds_read_b128 v[218:221], v207 offset:16384
	ds_read_b128 v[226:229], v207 offset:18432
	ds_read_b128 v[230:233], v206 offset:20480
	ds_read_b128 v[238:241], v206 offset:22528
	ds_read_b128 v[234:237], v207 offset:20480
	ds_read_b128 v[242:245], v207 offset:22528
	global_load_lds_dwordx4 v[186:187], off
	v_lshl_add_u64 v[188:189], s[28:29], 0, v[162:163]
	s_add_i32 m0, s63, 0x2000
	s_add_i32 s28, s48, s34
	global_load_lds_dwordx4 v[188:189], off
	v_lshl_add_u64 v[190:191], s[30:31], 0, v[160:161]
	s_mov_b32 m0, s28
	v_lshl_add_u64 v[192:193], s[30:31], 0, v[162:163]
	global_load_lds_dwordx4 v[190:191], off
	s_add_i32 m0, s28, 0x2000
	v_mov_b32_e32 v167, v165
	global_load_lds_dwordx4 v[192:193], off
	s_mov_b32 m0, s35
	v_lshl_add_u64 v[196:197], s[26:27], 0, v[164:165]
	global_load_lds_dwordx4 v164, s[26:27]
	s_mov_b32 m0, s36
	v_lshl_add_u64 v[194:195], s[26:27], 0, v[166:167]
	global_load_lds_dwordx4 v166, s[26:27]
	s_waitcnt vmcnt(8)
	s_waitcnt lgkmcnt(0)
	s_barrier
	s_setprio 1
	s_waitcnt lgkmcnt(0)
	v_mfma_f32_16x16x128_f8f6f4 v[92:95], v[24:31], v[214:221], v[92:95]
	v_mfma_f32_16x16x128_f8f6f4 v[88:91], v[16:23], v[214:221], v[88:91]
	v_mfma_f32_16x16x128_f8f6f4 v[80:83], v[24:31], v[222:229], v[80:83]
	v_mfma_f32_16x16x128_f8f6f4 v[72:75], v[16:23], v[222:229], v[72:75]
	v_mfma_f32_16x16x128_f8f6f4 v[60:63], v[24:31], v[230:237], v[60:63]
	v_mfma_f32_16x16x128_f8f6f4 v[56:59], v[16:23], v[230:237], v[56:59]
	v_mfma_f32_16x16x128_f8f6f4 v[48:51], v[24:31], v[238:245], v[48:51]
	v_mfma_f32_16x16x128_f8f6f4 v[40:43], v[16:23], v[238:245], v[40:43]
	v_mfma_f32_16x16x128_f8f6f4 v[84:87], v[8:15], v[214:221], v[84:87]
	v_mfma_f32_16x16x128_f8f6f4 v[76:79], v[0:7], v[214:221], v[76:79]
	v_mfma_f32_16x16x128_f8f6f4 v[68:71], v[8:15], v[222:229], v[68:71]
	v_mfma_f32_16x16x128_f8f6f4 v[64:67], v[0:7], v[222:229], v[64:67]
	v_mfma_f32_16x16x128_f8f6f4 v[52:55], v[8:15], v[230:237], v[52:55]
	v_mfma_f32_16x16x128_f8f6f4 v[44:47], v[0:7], v[230:237], v[44:47]
	v_mfma_f32_16x16x128_f8f6f4 v[36:39], v[8:15], v[238:245], v[36:39]
	v_mfma_f32_16x16x128_f8f6f4 v[32:35], v[0:7], v[238:245], v[32:35]
	s_setprio 0
	s_barrier
	s_add_i32 s28, 0, 0x18000
	s_add_i32 s29, 0, 0x1c000
	ds_read_b128 v[0:3], v252 offset:32768
	ds_read_b128 v[4:7], v253 offset:32768
	ds_read_b128 v[8:11], v252 offset:34816
	ds_read_b128 v[12:15], v253 offset:34816
	ds_read_b128 v[16:19], v252 offset:49152
	ds_read_b128 v[20:23], v253 offset:49152
	ds_read_b128 v[24:27], v252 offset:51200
	ds_read_b128 v[28:31], v253 offset:51200
	s_mov_b32 m0, s37
	v_lshl_add_u64 v[184:185], s[26:27], 0, v[184:185]
	ds_read_b128 v[214:217], v206 offset:32768
	ds_read_b128 v[222:225], v206 offset:34816
	ds_read_b128 v[218:221], v207 offset:32768
	ds_read_b128 v[226:229], v207 offset:34816
	ds_read_b128 v[230:233], v206 offset:36864
	ds_read_b128 v[238:241], v206 offset:38912
	ds_read_b128 v[234:237], v207 offset:36864
	ds_read_b128 v[242:245], v207 offset:38912
	global_load_lds_dwordx4 v[184:185], off
	v_lshl_add_u64 v[182:183], s[26:27], 0, v[182:183]
	s_mov_b32 m0, s38
	s_nop 0
	global_load_lds_dwordx4 v[182:183], off
	s_waitcnt vmcnt(8)
	s_waitcnt lgkmcnt(0)
	s_barrier
	s_setprio 1
	s_waitcnt lgkmcnt(0)
	v_mfma_f32_16x16x128_f8f6f4 v[156:159], v[0:7], v[214:221], v[156:159]
	v_mfma_f32_16x16x128_f8f6f4 v[152:155], v[8:15], v[214:221], v[152:155]
	v_mfma_f32_16x16x128_f8f6f4 v[144:147], v[0:7], v[222:229], v[144:147]
	v_mfma_f32_16x16x128_f8f6f4 v[136:139], v[8:15], v[222:229], v[136:139]
	v_mfma_f32_16x16x128_f8f6f4 v[124:127], v[0:7], v[230:237], v[124:127]
	v_mfma_f32_16x16x128_f8f6f4 v[120:123], v[8:15], v[230:237], v[120:123]
	v_mfma_f32_16x16x128_f8f6f4 v[112:115], v[0:7], v[238:245], v[112:115]
	v_mfma_f32_16x16x128_f8f6f4 v[104:107], v[8:15], v[238:245], v[104:107]
	v_mfma_f32_16x16x128_f8f6f4 v[148:151], v[16:23], v[214:221], v[148:151]
	v_mfma_f32_16x16x128_f8f6f4 v[140:143], v[24:31], v[214:221], v[140:143]
	v_mfma_f32_16x16x128_f8f6f4 v[132:135], v[16:23], v[222:229], v[132:135]
	v_mfma_f32_16x16x128_f8f6f4 v[128:131], v[24:31], v[222:229], v[128:131]
	v_mfma_f32_16x16x128_f8f6f4 v[116:119], v[16:23], v[230:237], v[116:119]
	v_mfma_f32_16x16x128_f8f6f4 v[108:111], v[24:31], v[230:237], v[108:111]
	v_mfma_f32_16x16x128_f8f6f4 v[100:103], v[16:23], v[238:245], v[100:103]
	v_mfma_f32_16x16x128_f8f6f4 v[96:99], v[24:31], v[238:245], v[96:99]
	s_setprio 0
	s_barrier
	s_add_i32 s26, s28, s34
	v_lshl_add_u64 v[182:183], v[186:187], 0, s[12:13]
	s_mov_b32 m0, s26
	ds_read_b128 v[214:217], v206 offset:49152
	ds_read_b128 v[222:225], v206 offset:51200
	ds_read_b128 v[218:221], v207 offset:49152
	ds_read_b128 v[226:229], v207 offset:51200
	ds_read_b128 v[230:233], v206 offset:53248
	ds_read_b128 v[238:241], v206 offset:55296
	ds_read_b128 v[234:237], v207 offset:53248
	ds_read_b128 v[242:245], v207 offset:55296
	global_load_lds_dwordx4 v[182:183], off
	v_lshl_add_u64 v[182:183], v[188:189], 0, s[12:13]
	s_add_i32 m0, s26, 0x2000
	s_add_i32 s26, s29, s34
	global_load_lds_dwordx4 v[182:183], off
	v_lshl_add_u64 v[182:183], v[190:191], 0, s[12:13]
	s_mov_b32 m0, s26
	s_nop 0
	global_load_lds_dwordx4 v[182:183], off
	v_lshl_add_u64 v[182:183], v[192:193], 0, s[12:13]
	s_add_i32 m0, s26, 0x2000
	s_nop 0
	global_load_lds_dwordx4 v[182:183], off
	v_lshl_add_u64 v[182:183], v[196:197], 0, s[12:13]
	s_mov_b32 m0, s41
	s_nop 0
	global_load_lds_dwordx4 v[182:183], off
	v_lshl_add_u64 v[182:183], v[194:195], 0, s[12:13]
	s_mov_b32 m0, s42
	s_nop 0
	global_load_lds_dwordx4 v[182:183], off
	s_waitcnt vmcnt(8)
	s_waitcnt lgkmcnt(0)
	s_barrier
	s_setprio 1
	s_waitcnt lgkmcnt(0)
	v_mfma_f32_16x16x128_f8f6f4 v[92:95], v[0:7], v[214:221], v[92:95]
	v_mfma_f32_16x16x128_f8f6f4 v[88:91], v[8:15], v[214:221], v[88:91]
	v_mfma_f32_16x16x128_f8f6f4 v[80:83], v[0:7], v[222:229], v[80:83]
	v_mfma_f32_16x16x128_f8f6f4 v[72:75], v[8:15], v[222:229], v[72:75]
	v_mfma_f32_16x16x128_f8f6f4 v[60:63], v[0:7], v[230:237], v[60:63]
	v_mfma_f32_16x16x128_f8f6f4 v[56:59], v[8:15], v[230:237], v[56:59]
	v_mfma_f32_16x16x128_f8f6f4 v[48:51], v[0:7], v[238:245], v[48:51]
	v_mfma_f32_16x16x128_f8f6f4 v[40:43], v[8:15], v[238:245], v[40:43]
	v_mfma_f32_16x16x128_f8f6f4 v[84:87], v[16:23], v[214:221], v[84:87]
	v_mfma_f32_16x16x128_f8f6f4 v[76:79], v[24:31], v[214:221], v[76:79]
	v_mfma_f32_16x16x128_f8f6f4 v[68:71], v[16:23], v[222:229], v[68:71]
	v_mfma_f32_16x16x128_f8f6f4 v[64:67], v[24:31], v[222:229], v[64:67]
	v_mfma_f32_16x16x128_f8f6f4 v[52:55], v[16:23], v[230:237], v[52:55]
	v_mfma_f32_16x16x128_f8f6f4 v[44:47], v[24:31], v[230:237], v[44:47]
	v_mfma_f32_16x16x128_f8f6f4 v[36:39], v[16:23], v[238:245], v[36:39]
	v_mfma_f32_16x16x128_f8f6f4 v[32:35], v[24:31], v[238:245], v[32:35]
	s_setprio 0
	s_barrier
	s_add_i32 s62, s62, 2
	s_add_u32 s24, s24, 0x100
	s_addc_u32 s25, s25, 0
	s_cmp_gt_u32 s62, 29
	s_cbranch_scc1 .LBB0_1552
